# waves 4-7 pre-softmax sleep s_sleep 7 (stagger-offset tuning, one step past the previous setting)
# baseline (speedup 1.0000x reference)
.LBB0_517:
	s_or_b64 exec, exec, s[4:5]
	s_lshr_b32 s3, s2, 1
	s_mul_i32 s3, s15, s3
	v_readlane_b32 s4, v255, 16
	s_add_i32 s33, s4, s3
	s_lshl_b32 s3, s33, 7
	s_and_b32 s6, s3, 0xfffff000
	s_lshl_b32 s3, s33, 8
	s_ashr_i32 s82, s33, 3
	s_and_b32 s3, s3, 0x700
	s_and_b32 s2, s2, 1
	s_and_b32 s69, s82, 3
	s_xor_b32 s4, s3, 0xf00
	s_cmp_eq_u32 s2, 0
	s_mov_b32 s2, s6
	s_cselect_b32 s84, s4, s3
	v_writelane_b32 v255, s2, 46
	s_ashr_i32 s7, s6, 31
	s_lshl_b64 s[66:67], s[6:7], 11
	v_writelane_b32 v255, s3, 47
	v_mov_b32_e32 v0, v165
	v_readlane_b32 s2, v255, 25
	s_add_u32 s2, s2, s66
	v_readlane_b32 s3, v255, 26
	s_addc_u32 s3, s3, s67
	s_lshl_b32 s4, s69, 8
	s_add_u32 s6, s2, s4
	s_addc_u32 s7, s3, 0
	s_add_u32 s3, s6, 0x400
	v_writelane_b32 v255, s4, 48
	s_addc_u32 s68, s7, 0
	s_ashr_i32 s83, s82, 31
	s_lshl_b64 s[4:5], s[82:83], 14
	v_readlane_b32 s2, v255, 17
	s_add_u32 s8, s2, s4
	v_readlane_b32 s2, v255, 18
	s_addc_u32 s9, s2, s5
	s_lshl_b32 s4, s82, 6
	s_ashr_i32 s5, s4, 31
	s_lshl_b64 s[4:5], s[4:5], 2
	v_readlane_b32 s2, v255, 21
	s_add_u32 s4, s2, s4
	v_readlane_b32 s2, v255, 22
	s_addc_u32 s5, s2, s5
	v_mov_b32_e32 v3, v161
	v_readfirstlane_b32 s2, v0
	s_ashr_i32 s10, s2, 6
	s_lshl_b32 s12, s10, 5
	s_mov_b32 s2, s12
	v_and_b32_e32 v39, 63, v0
	v_writelane_b32 v255, s2, 49
	s_add_i32 s94, s12, s84
	v_lshlrev_b32_e32 v2, 2, v39
	v_writelane_b32 v255, s3, 50
	s_lshl_b32 s2, s10, 11
	v_lshl_add_u64 v[4:5], s[4:5], 0, v[2:3]
	v_readlane_b32 s11, v255, 28
	s_lshl_b32 s4, s10, 12
	s_ashr_i32 s95, s94, 31
	s_lshl_b32 s78, s10, 3
	flat_load_dword v3, v[4:5]
	s_add_i32 s2, s2, s11
	s_add_i32 s81, s4, s79
	s_lshl_b64 s[12:13], s[94:95], 2
	v_and_b32_e32 v175, 31, v0
	s_add_u32 s4, s8, s12
	v_writelane_b32 v255, s12, 51
	s_addc_u32 s5, s9, s13
	v_lshlrev_b32_e32 v160, 2, v175
	v_lshl_add_u64 v[4:5], s[4:5], 0, v[160:161]
	flat_load_dword v178, v[4:5]
	v_bfe_u32 v4, v0, 4, 2
	v_bitop3_b32 v6, v4, v0, 15 bitop3:0x78
	v_add_u32_e32 v2, s89, v2
	v_writelane_b32 v255, s13, 52
	v_bfe_u32 v176, v0, 5, 1
	v_lshlrev_b32_e32 v6, 4, v6
	v_or_b32_e32 v4, s78, v4
	v_and_b32_e32 v5, 15, v0
	v_lshlrev_b32_e32 v1, 2, v176
	s_mulk_i32 s10, 0x1c00
	v_lshl_or_b32 v170, v4, 11, v6
	v_or_b32_e32 v4, 4, v4
	v_readlane_b32 s4, v255, 33
	v_lshlrev_b32_e32 v40, 4, v39
	v_sub_u32_e32 v7, v175, v1
	v_bitop3_b32 v5, v4, v5, 7 bitop3:0x6c
	v_lshlrev_b32_e32 v4, 11, v4
	s_add_i32 s4, s4, s10
	v_add_u32_e32 v180, s94, v7
	v_lshl_or_b32 v172, v5, 4, v4
	v_add_u32_e32 v181, s4, v40
	v_lshlrev_b32_e32 v174, 4, v176
	s_waitcnt vmcnt(0) lgkmcnt(0)
	ds_write_b32 v2, v3
	s_waitcnt vmcnt(0)
	ds_write_b128 v181, v[128:131]
	ds_write_b128 v181, v[132:135] offset:1024
	ds_write_b128 v181, v[136:139] offset:2048
	ds_write_b128 v181, v[140:143] offset:3072
	ds_write_b128 v181, v[144:147] offset:4096
	ds_write_b128 v181, v[148:151] offset:5120
	ds_write_b128 v181, v[152:155] offset:6144
	s_add_u32 s4, s6, 0x20400
	s_addc_u32 s5, s7, 0
	v_mov_b32_e32 v171, v161
	v_lshl_add_u64 v[2:3], s[4:5], 0, v[170:171]
	s_add_i32 s96, s2, 0x4000
	s_mov_b32 s6, m0
	s_mov_b32 m0, s96
	s_nop 0
	global_load_lds_dwordx4 v[2:3], off
	s_mov_b32 m0, s6
	v_mov_b32_e32 v173, v161
	v_lshl_add_u64 v[2:3], s[4:5], 0, v[172:173]
	s_add_i32 s97, s2, 0x4400
	s_mov_b32 s4, m0
	s_mov_b32 m0, s97
	s_nop 0
	global_load_lds_dwordx4 v[2:3], off
	s_mov_b32 m0, s4
	s_waitcnt lgkmcnt(0)
	s_barrier
	v_lshlrev_b32_e32 v2, 4, v0
	s_movk_i32 s4, 0x70
	v_lshlrev_b32_e32 v34, 8, v175
	v_and_b32_e32 v3, 0x70, v2
	v_bitop3_b32 v35, v174, v2, s4 bitop3:0x78
	s_movk_i32 s4, 0x60
	v_add_u32_e32 v4, s11, v34
	v_bitop3_b32 v36, v174, v3, 32 bitop3:0x36
	v_bitop3_b32 v37, v174, v3, 64 bitop3:0x36
	v_bitop3_b32 v38, v174, v3, s4 bitop3:0x36
	v_add_u32_e32 v182, v35, v4
	v_add_u32_e32 v183, v36, v4
	v_add_u32_e32 v184, v37, v4
	v_add_u32_e32 v185, v38, v4
	ds_read_b128 v[2:5], v182 offset:0
	ds_read_b128 v[6:9], v182 offset:0x2000
	ds_read_b128 v[10:13], v181 offset:0
	ds_read_b128 v[42:45], v183 offset:0
	ds_read_b128 v[46:49], v183 offset:0x2000
	ds_read_b128 v[50:53], v181 offset:0x400
	s_waitcnt lgkmcnt(3)
	s_nop 0
	v_mfma_f32_32x32x16_bf16 v[18:33], v[2:5], v[10:13], 0
	v_mfma_f32_32x32x16_bf16 v[2:17], v[6:9], v[10:13], 0
	ds_read_b128 v[54:57], v184 offset:0
	ds_read_b128 v[58:61], v184 offset:0x2000
	ds_read_b128 v[62:65], v181 offset:0x800
	s_waitcnt lgkmcnt(3)
	v_mfma_f32_32x32x16_bf16 v[18:33], v[42:45], v[50:53], v[18:33]
	v_mfma_f32_32x32x16_bf16 v[2:17], v[46:49], v[50:53], v[2:17]
	ds_read_b128 v[42:45], v185 offset:0
	ds_read_b128 v[46:49], v185 offset:0x2000
	ds_read_b128 v[50:53], v181 offset:0xc00
	s_waitcnt lgkmcnt(3)
	v_mfma_f32_32x32x16_bf16 v[18:33], v[54:57], v[62:65], v[18:33]
	v_mfma_f32_32x32x16_bf16 v[2:17], v[58:61], v[62:65], v[2:17]
	ds_read_b128 v[54:57], v182 offset:0x80
	ds_read_b128 v[58:61], v182 offset:0x2080
	ds_read_b128 v[62:65], v181 offset:0x1000
	s_waitcnt lgkmcnt(3)
	v_mfma_f32_32x32x16_bf16 v[18:33], v[42:45], v[50:53], v[18:33]
	v_mfma_f32_32x32x16_bf16 v[2:17], v[46:49], v[50:53], v[2:17]
	ds_read_b128 v[42:45], v183 offset:0x80
	ds_read_b128 v[46:49], v183 offset:0x2080
	ds_read_b128 v[50:53], v181 offset:0x1400
	s_waitcnt lgkmcnt(3)
	v_mfma_f32_32x32x16_bf16 v[18:33], v[54:57], v[62:65], v[18:33]
	v_mfma_f32_32x32x16_bf16 v[2:17], v[58:61], v[62:65], v[2:17]
	ds_read_b128 v[54:57], v184 offset:0x80
	ds_read_b128 v[58:61], v184 offset:0x2080
	ds_read_b128 v[62:65], v181 offset:0x1800
	s_waitcnt lgkmcnt(3)
	v_mfma_f32_32x32x16_bf16 v[18:33], v[42:45], v[50:53], v[18:33]
	v_mfma_f32_32x32x16_bf16 v[2:17], v[46:49], v[50:53], v[2:17]
	ds_read_b128 v[42:45], v185 offset:0x80
	ds_read_b128 v[46:49], v185 offset:0x2080
	s_waitcnt lgkmcnt(2)
	v_mfma_f32_32x32x16_bf16 v[18:33], v[54:57], v[62:65], v[18:33]
	v_mfma_f32_32x32x16_bf16 v[2:17], v[58:61], v[62:65], v[2:17]
	s_waitcnt lgkmcnt(0)
	v_mfma_f32_32x32x16_bf16 v[18:33], v[42:45], v[166:169], v[18:33]
	v_mfma_f32_32x32x16_bf16 v[2:17], v[46:49], v[166:169], v[2:17]
	s_bitcmp0_b32 s100, 8
	s_cbranch_scc1 .Lstg_a1
	s_waitcnt vmcnt(0)
	s_waitcnt lgkmcnt(0)
	s_barrier
	s_sleep 7

.LBB0_520:
	ds_read_b64_tr_b16 v[144:145], v177 offset:0
	ds_read_b64_tr_b16 v[146:147], v177 offset:0x1000
	ds_read_b64_tr_b16 v[148:149], v177 offset:0x2000
	ds_read_b64_tr_b16 v[150:151], v177 offset:0x3000
	ds_read_b64_tr_b16 v[152:153], v177 offset:0x4000
	ds_read_b64_tr_b16 v[154:155], v177 offset:0x5000
	ds_read_b64_tr_b16 v[156:157], v177 offset:0x6000
	ds_read_b64_tr_b16 v[158:159], v177 offset:0x7000
	s_waitcnt lgkmcnt(6)
	s_nop 0
	v_mfma_f32_32x32x16_bf16 v[112:127], v[144:147], v[128:131], v[112:127]
	ds_read_b64_tr_b16 v[198:199], v177 offset:0x200
	ds_read_b64_tr_b16 v[200:201], v177 offset:0x1200
	s_waitcnt lgkmcnt(6)
	v_mfma_f32_32x32x16_bf16 v[112:127], v[148:151], v[132:135], v[112:127]
	ds_read_b64_tr_b16 v[202:203], v177 offset:0x2200
	ds_read_b64_tr_b16 v[204:205], v177 offset:0x3200
	s_waitcnt lgkmcnt(6)
	v_mfma_f32_32x32x16_bf16 v[112:127], v[152:155], v[136:139], v[112:127]
	ds_read_b64_tr_b16 v[206:207], v177 offset:0x4200
	ds_read_b64_tr_b16 v[208:209], v177 offset:0x5200
	s_waitcnt lgkmcnt(6)
	v_mfma_f32_32x32x16_bf16 v[112:127], v[156:159], v[140:143], v[112:127]
	ds_read_b64_tr_b16 v[210:211], v177 offset:0x6200
	ds_read_b64_tr_b16 v[212:213], v177 offset:0x7200
	s_waitcnt lgkmcnt(6)
	v_mfma_f32_32x32x16_bf16 v[0:15], v[198:201], v[128:131], v[0:15]
	ds_read_b64_tr_b16 v[144:145], v177 offset:0x400
	ds_read_b64_tr_b16 v[146:147], v177 offset:0x1400
	s_waitcnt lgkmcnt(6)
	v_mfma_f32_32x32x16_bf16 v[0:15], v[202:205], v[132:135], v[0:15]
	ds_read_b64_tr_b16 v[148:149], v177 offset:0x2400
	ds_read_b64_tr_b16 v[150:151], v177 offset:0x3400
	s_waitcnt lgkmcnt(6)
	v_mfma_f32_32x32x16_bf16 v[0:15], v[206:209], v[136:139], v[0:15]
	ds_read_b64_tr_b16 v[152:153], v177 offset:0x4400
	ds_read_b64_tr_b16 v[154:155], v177 offset:0x5400
	s_waitcnt lgkmcnt(6)
	v_mfma_f32_32x32x16_bf16 v[0:15], v[210:213], v[140:143], v[0:15]
	ds_read_b64_tr_b16 v[156:157], v177 offset:0x6400
	ds_read_b64_tr_b16 v[158:159], v177 offset:0x7400
	s_waitcnt lgkmcnt(6)
	v_mfma_f32_32x32x16_bf16 v[16:31], v[144:147], v[128:131], v[16:31]
	ds_read_b64_tr_b16 v[198:199], v177 offset:0x600
	ds_read_b64_tr_b16 v[200:201], v177 offset:0x1600
	s_waitcnt lgkmcnt(6)
	v_mfma_f32_32x32x16_bf16 v[16:31], v[148:151], v[132:135], v[16:31]
	ds_read_b64_tr_b16 v[202:203], v177 offset:0x2600
	ds_read_b64_tr_b16 v[204:205], v177 offset:0x3600
	s_waitcnt lgkmcnt(6)
	v_mfma_f32_32x32x16_bf16 v[16:31], v[152:155], v[136:139], v[16:31]
	ds_read_b64_tr_b16 v[206:207], v177 offset:0x4600
	ds_read_b64_tr_b16 v[208:209], v177 offset:0x5600
	s_waitcnt lgkmcnt(6)
	v_mfma_f32_32x32x16_bf16 v[16:31], v[156:159], v[140:143], v[16:31]
	ds_read_b64_tr_b16 v[210:211], v177 offset:0x6600
	ds_read_b64_tr_b16 v[212:213], v177 offset:0x7600
	s_waitcnt lgkmcnt(6)
	v_mfma_f32_32x32x16_bf16 v[32:47], v[198:201], v[128:131], v[32:47]
	ds_read_b64_tr_b16 v[144:145], v177 offset:0x800
	ds_read_b64_tr_b16 v[146:147], v177 offset:0x1800
	s_waitcnt lgkmcnt(6)
	v_mfma_f32_32x32x16_bf16 v[32:47], v[202:205], v[132:135], v[32:47]
	ds_read_b64_tr_b16 v[148:149], v177 offset:0x2800
	ds_read_b64_tr_b16 v[150:151], v177 offset:0x3800
	s_waitcnt lgkmcnt(6)
	v_mfma_f32_32x32x16_bf16 v[32:47], v[206:209], v[136:139], v[32:47]
	ds_read_b64_tr_b16 v[152:153], v177 offset:0x4800
	ds_read_b64_tr_b16 v[154:155], v177 offset:0x5800
	s_waitcnt lgkmcnt(6)
	v_mfma_f32_32x32x16_bf16 v[32:47], v[210:213], v[140:143], v[32:47]
	ds_read_b64_tr_b16 v[156:157], v177 offset:0x6800
	ds_read_b64_tr_b16 v[158:159], v177 offset:0x7800
	s_waitcnt lgkmcnt(6)
	v_mfma_f32_32x32x16_bf16 v[48:63], v[144:147], v[128:131], v[48:63]
	ds_read_b64_tr_b16 v[198:199], v177 offset:0xa00
	ds_read_b64_tr_b16 v[200:201], v177 offset:0x1a00
	s_waitcnt lgkmcnt(6)
	v_mfma_f32_32x32x16_bf16 v[48:63], v[148:151], v[132:135], v[48:63]
	ds_read_b64_tr_b16 v[202:203], v177 offset:0x2a00
	ds_read_b64_tr_b16 v[204:205], v177 offset:0x3a00
	s_waitcnt lgkmcnt(6)
	v_mfma_f32_32x32x16_bf16 v[48:63], v[152:155], v[136:139], v[48:63]
	ds_read_b64_tr_b16 v[206:207], v177 offset:0x4a00
	ds_read_b64_tr_b16 v[208:209], v177 offset:0x5a00
	s_waitcnt lgkmcnt(6)
	v_mfma_f32_32x32x16_bf16 v[48:63], v[156:159], v[140:143], v[48:63]
	ds_read_b64_tr_b16 v[210:211], v177 offset:0x6a00
	ds_read_b64_tr_b16 v[212:213], v177 offset:0x7a00
	s_waitcnt lgkmcnt(6)
	v_mfma_f32_32x32x16_bf16 v[64:79], v[198:201], v[128:131], v[64:79]
	ds_read_b64_tr_b16 v[144:145], v177 offset:0xc00
	ds_read_b64_tr_b16 v[146:147], v177 offset:0x1c00
	s_waitcnt lgkmcnt(6)
	v_mfma_f32_32x32x16_bf16 v[64:79], v[202:205], v[132:135], v[64:79]
	ds_read_b64_tr_b16 v[148:149], v177 offset:0x2c00
	ds_read_b64_tr_b16 v[150:151], v177 offset:0x3c00
	s_waitcnt lgkmcnt(6)
	v_mfma_f32_32x32x16_bf16 v[64:79], v[206:209], v[136:139], v[64:79]
	ds_read_b64_tr_b16 v[152:153], v177 offset:0x4c00
	ds_read_b64_tr_b16 v[154:155], v177 offset:0x5c00
	s_waitcnt lgkmcnt(6)
	v_mfma_f32_32x32x16_bf16 v[64:79], v[210:213], v[140:143], v[64:79]
	ds_read_b64_tr_b16 v[156:157], v177 offset:0x6c00
	ds_read_b64_tr_b16 v[158:159], v177 offset:0x7c00
	s_waitcnt lgkmcnt(6)
	v_mfma_f32_32x32x16_bf16 v[80:95], v[144:147], v[128:131], v[80:95]
	ds_read_b64_tr_b16 v[198:199], v177 offset:0xe00
	ds_read_b64_tr_b16 v[200:201], v177 offset:0x1e00
	s_waitcnt lgkmcnt(6)
	v_mfma_f32_32x32x16_bf16 v[80:95], v[148:151], v[132:135], v[80:95]
	ds_read_b64_tr_b16 v[202:203], v177 offset:0x2e00
	ds_read_b64_tr_b16 v[204:205], v177 offset:0x3e00
	s_waitcnt lgkmcnt(6)
	v_mfma_f32_32x32x16_bf16 v[80:95], v[152:155], v[136:139], v[80:95]
	ds_read_b64_tr_b16 v[206:207], v177 offset:0x4e00
	ds_read_b64_tr_b16 v[208:209], v177 offset:0x5e00
	s_waitcnt lgkmcnt(6)
	v_mfma_f32_32x32x16_bf16 v[80:95], v[156:159], v[140:143], v[80:95]
	ds_read_b64_tr_b16 v[210:211], v177 offset:0x6e00
	ds_read_b64_tr_b16 v[212:213], v177 offset:0x7e00
	s_waitcnt lgkmcnt(6)
	v_mfma_f32_32x32x16_bf16 v[96:111], v[198:201], v[128:131], v[96:111]
	s_waitcnt lgkmcnt(4)
	v_mfma_f32_32x32x16_bf16 v[96:111], v[202:205], v[132:135], v[96:111]
	s_waitcnt lgkmcnt(2)
	v_mfma_f32_32x32x16_bf16 v[96:111], v[206:209], v[136:139], v[96:111]
	s_waitcnt lgkmcnt(0)
	v_mfma_f32_32x32x16_bf16 v[96:111], v[210:213], v[140:143], v[96:111]
	ds_read_b128 v[128:131], v189 offset:0
	ds_read_b128 v[132:135], v189 offset:0x2000
	ds_read_b128 v[136:139], v181 offset:0
	ds_read_b128 v[198:201], v188 offset:0
	ds_read_b128 v[202:205], v188 offset:0x2000
	ds_read_b128 v[206:209], v181 offset:0x400
	s_waitcnt lgkmcnt(3)
	s_nop 0
	v_mfma_f32_32x32x16_bf16 v[144:159], v[128:131], v[136:139], 0
	v_mfma_f32_32x32x16_bf16 v[128:143], v[132:135], v[136:139], 0
	ds_read_b128 v[210:213], v187 offset:0
	ds_read_b128 v[214:217], v187 offset:0x2000
	ds_read_b128 v[218:221], v181 offset:0x800
	s_waitcnt lgkmcnt(3)
	v_mfma_f32_32x32x16_bf16 v[144:159], v[198:201], v[206:209], v[144:159]
	v_mfma_f32_32x32x16_bf16 v[128:143], v[202:205], v[206:209], v[128:143]
	ds_read_b128 v[198:201], v186 offset:0
	ds_read_b128 v[202:205], v186 offset:0x2000
	ds_read_b128 v[206:209], v181 offset:0xc00
	s_waitcnt lgkmcnt(3)
	v_mfma_f32_32x32x16_bf16 v[144:159], v[210:213], v[218:221], v[144:159]
	v_mfma_f32_32x32x16_bf16 v[128:143], v[214:217], v[218:221], v[128:143]
	ds_read_b128 v[210:213], v189 offset:0x80
	ds_read_b128 v[214:217], v189 offset:0x2080
	ds_read_b128 v[218:221], v181 offset:0x1000
	s_waitcnt lgkmcnt(3)
	v_mfma_f32_32x32x16_bf16 v[144:159], v[198:201], v[206:209], v[144:159]
	v_mfma_f32_32x32x16_bf16 v[128:143], v[202:205], v[206:209], v[128:143]
	ds_read_b128 v[198:201], v188 offset:0x80
	ds_read_b128 v[202:205], v188 offset:0x2080
	ds_read_b128 v[206:209], v181 offset:0x1400
	s_waitcnt lgkmcnt(3)
	v_mfma_f32_32x32x16_bf16 v[144:159], v[210:213], v[218:221], v[144:159]
	v_mfma_f32_32x32x16_bf16 v[128:143], v[214:217], v[218:221], v[128:143]
	ds_read_b128 v[210:213], v187 offset:0x80
	ds_read_b128 v[214:217], v187 offset:0x2080
	ds_read_b128 v[218:221], v181 offset:0x1800
	s_waitcnt lgkmcnt(3)
	v_mfma_f32_32x32x16_bf16 v[144:159], v[198:201], v[206:209], v[144:159]
	v_mfma_f32_32x32x16_bf16 v[128:143], v[202:205], v[206:209], v[128:143]
	ds_read_b128 v[198:201], v186 offset:0x80
	ds_read_b128 v[202:205], v186 offset:0x2080
	s_waitcnt lgkmcnt(2)
	v_mfma_f32_32x32x16_bf16 v[144:159], v[210:213], v[218:221], v[144:159]
	v_mfma_f32_32x32x16_bf16 v[128:143], v[214:217], v[218:221], v[128:143]
	s_waitcnt lgkmcnt(0)
	v_mfma_f32_32x32x16_bf16 v[144:159], v[198:201], v[166:169], v[144:159]
	v_mfma_f32_32x32x16_bf16 v[128:143], v[202:205], v[166:169], v[128:143]
	s_bitcmp0_b32 s100, 8
	s_cbranch_scc1 .Lstg_a2
	s_waitcnt vmcnt(0)
	s_waitcnt lgkmcnt(0)
	s_barrier
	s_sleep 7

.LBB0_526:
	s_add_u32 s33, s72, s84
	s_addc_u32 s92, s73, s90
	s_add_u32 s4, s33, 0x2dd40800
	s_addc_u32 s5, s92, 0
	s_mov_b32 m0, s81
	s_nop 0
	global_load_lds_dwordx4 v162, s[4:5]
	s_add_i32 m0, s78, 0xffffff80
	s_nop 0
	global_load_lds_dwordx4 v162, s[4:5] offset:128
	s_add_i32 m0, s69, 0xffffff00
	s_nop 0
	global_load_lds_dwordx4 v162, s[4:5] offset:256
	s_add_i32 m0, s68, 0xfffffe80
	s_nop 0
	global_load_lds_dwordx4 v162, s[4:5] offset:384
	ds_read_b64_tr_b16 v[144:145], v177 offset:0x8000
	ds_read_b64_tr_b16 v[146:147], v177 offset:0x9000
	ds_read_b64_tr_b16 v[148:149], v177 offset:0xa000
	ds_read_b64_tr_b16 v[150:151], v177 offset:0xb000
	ds_read_b64_tr_b16 v[152:153], v177 offset:0xc000
	ds_read_b64_tr_b16 v[154:155], v177 offset:0xd000
	ds_read_b64_tr_b16 v[156:157], v177 offset:0xe000
	ds_read_b64_tr_b16 v[158:159], v177 offset:0xf000
	s_waitcnt lgkmcnt(6)
	s_nop 1
	v_mfma_f32_32x32x16_bf16 v[112:127], v[144:147], v[128:131], v[112:127]
	ds_read_b64_tr_b16 v[236:237], v177 offset:0x8200
	ds_read_b64_tr_b16 v[238:239], v177 offset:0x9200
	s_waitcnt lgkmcnt(6)
	v_mfma_f32_32x32x16_bf16 v[112:127], v[148:151], v[132:135], v[112:127]
	ds_read_b64_tr_b16 v[240:241], v177 offset:0xa200
	ds_read_b64_tr_b16 v[242:243], v177 offset:0xb200
	s_waitcnt lgkmcnt(6)
	v_mfma_f32_32x32x16_bf16 v[112:127], v[152:155], v[136:139], v[112:127]
	ds_read_b64_tr_b16 v[244:245], v177 offset:0xc200
	ds_read_b64_tr_b16 v[246:247], v177 offset:0xd200
	s_waitcnt lgkmcnt(6)
	v_mfma_f32_32x32x16_bf16 v[112:127], v[156:159], v[140:143], v[112:127]
	ds_read_b64_tr_b16 v[248:249], v177 offset:0xe200
	ds_read_b64_tr_b16 v[250:251], v177 offset:0xf200
	s_waitcnt lgkmcnt(6)
	v_mfma_f32_32x32x16_bf16 v[0:15], v[236:239], v[128:131], v[0:15]
	ds_read_b64_tr_b16 v[144:145], v177 offset:0x8400
	ds_read_b64_tr_b16 v[146:147], v177 offset:0x9400
	s_waitcnt lgkmcnt(6)
	v_mfma_f32_32x32x16_bf16 v[0:15], v[240:243], v[132:135], v[0:15]
	ds_read_b64_tr_b16 v[148:149], v177 offset:0xa400
	ds_read_b64_tr_b16 v[150:151], v177 offset:0xb400
	s_waitcnt lgkmcnt(6)
	v_mfma_f32_32x32x16_bf16 v[0:15], v[244:247], v[136:139], v[0:15]
	ds_read_b64_tr_b16 v[152:153], v177 offset:0xc400
	ds_read_b64_tr_b16 v[154:155], v177 offset:0xd400
	s_waitcnt lgkmcnt(6)
	v_mfma_f32_32x32x16_bf16 v[0:15], v[248:251], v[140:143], v[0:15]
	ds_read_b64_tr_b16 v[156:157], v177 offset:0xe400
	ds_read_b64_tr_b16 v[158:159], v177 offset:0xf400
	s_waitcnt lgkmcnt(6)
	v_mfma_f32_32x32x16_bf16 v[16:31], v[144:147], v[128:131], v[16:31]
	ds_read_b64_tr_b16 v[236:237], v177 offset:0x8600
	ds_read_b64_tr_b16 v[238:239], v177 offset:0x9600
	s_waitcnt lgkmcnt(6)
	v_mfma_f32_32x32x16_bf16 v[16:31], v[148:151], v[132:135], v[16:31]
	ds_read_b64_tr_b16 v[240:241], v177 offset:0xa600
	ds_read_b64_tr_b16 v[242:243], v177 offset:0xb600
	s_waitcnt lgkmcnt(6)
	v_mfma_f32_32x32x16_bf16 v[16:31], v[152:155], v[136:139], v[16:31]
	ds_read_b64_tr_b16 v[244:245], v177 offset:0xc600
	ds_read_b64_tr_b16 v[246:247], v177 offset:0xd600
	s_waitcnt lgkmcnt(6)
	v_mfma_f32_32x32x16_bf16 v[16:31], v[156:159], v[140:143], v[16:31]
	ds_read_b64_tr_b16 v[248:249], v177 offset:0xe600
	ds_read_b64_tr_b16 v[250:251], v177 offset:0xf600
	s_waitcnt lgkmcnt(6)
	v_mfma_f32_32x32x16_bf16 v[32:47], v[236:239], v[128:131], v[32:47]
	ds_read_b64_tr_b16 v[144:145], v177 offset:0x8800
	ds_read_b64_tr_b16 v[146:147], v177 offset:0x9800
	s_waitcnt lgkmcnt(6)
	v_mfma_f32_32x32x16_bf16 v[32:47], v[240:243], v[132:135], v[32:47]
	ds_read_b64_tr_b16 v[148:149], v177 offset:0xa800
	ds_read_b64_tr_b16 v[150:151], v177 offset:0xb800
	s_waitcnt lgkmcnt(6)
	v_mfma_f32_32x32x16_bf16 v[32:47], v[244:247], v[136:139], v[32:47]
	ds_read_b64_tr_b16 v[152:153], v177 offset:0xc800
	ds_read_b64_tr_b16 v[154:155], v177 offset:0xd800
	s_waitcnt lgkmcnt(6)
	v_mfma_f32_32x32x16_bf16 v[32:47], v[248:251], v[140:143], v[32:47]
	ds_read_b64_tr_b16 v[156:157], v177 offset:0xe800
	ds_read_b64_tr_b16 v[158:159], v177 offset:0xf800
	s_waitcnt lgkmcnt(6)
	v_mfma_f32_32x32x16_bf16 v[48:63], v[144:147], v[128:131], v[48:63]
	ds_read_b64_tr_b16 v[236:237], v177 offset:0x8a00
	ds_read_b64_tr_b16 v[238:239], v177 offset:0x9a00
	s_waitcnt lgkmcnt(6)
	v_mfma_f32_32x32x16_bf16 v[48:63], v[148:151], v[132:135], v[48:63]
	ds_read_b64_tr_b16 v[240:241], v177 offset:0xaa00
	ds_read_b64_tr_b16 v[242:243], v177 offset:0xba00
	s_waitcnt lgkmcnt(6)
	v_mfma_f32_32x32x16_bf16 v[48:63], v[152:155], v[136:139], v[48:63]
	ds_read_b64_tr_b16 v[244:245], v177 offset:0xca00
	ds_read_b64_tr_b16 v[246:247], v177 offset:0xda00
	s_waitcnt lgkmcnt(6)
	v_mfma_f32_32x32x16_bf16 v[48:63], v[156:159], v[140:143], v[48:63]
	ds_read_b64_tr_b16 v[248:249], v177 offset:0xea00
	ds_read_b64_tr_b16 v[250:251], v177 offset:0xfa00
	s_waitcnt lgkmcnt(6)
	v_mfma_f32_32x32x16_bf16 v[64:79], v[236:239], v[128:131], v[64:79]
	ds_read_b64_tr_b16 v[144:145], v177 offset:0x8c00
	ds_read_b64_tr_b16 v[146:147], v177 offset:0x9c00
	s_waitcnt lgkmcnt(6)
	v_mfma_f32_32x32x16_bf16 v[64:79], v[240:243], v[132:135], v[64:79]
	ds_read_b64_tr_b16 v[148:149], v177 offset:0xac00
	ds_read_b64_tr_b16 v[150:151], v177 offset:0xbc00
	s_waitcnt lgkmcnt(6)
	v_mfma_f32_32x32x16_bf16 v[64:79], v[244:247], v[136:139], v[64:79]
	ds_read_b64_tr_b16 v[152:153], v177 offset:0xcc00
	ds_read_b64_tr_b16 v[154:155], v177 offset:0xdc00
	s_waitcnt lgkmcnt(6)
	v_mfma_f32_32x32x16_bf16 v[64:79], v[248:251], v[140:143], v[64:79]
	ds_read_b64_tr_b16 v[156:157], v177 offset:0xec00
	ds_read_b64_tr_b16 v[158:159], v177 offset:0xfc00
	s_waitcnt lgkmcnt(6)
	v_mfma_f32_32x32x16_bf16 v[80:95], v[144:147], v[128:131], v[80:95]
	ds_read_b64_tr_b16 v[236:237], v177 offset:0x8e00
	ds_read_b64_tr_b16 v[238:239], v177 offset:0x9e00
	s_waitcnt lgkmcnt(6)
	v_mfma_f32_32x32x16_bf16 v[80:95], v[148:151], v[132:135], v[80:95]
	ds_read_b64_tr_b16 v[240:241], v177 offset:0xae00
	ds_read_b64_tr_b16 v[242:243], v177 offset:0xbe00
	s_waitcnt lgkmcnt(6)
	v_mfma_f32_32x32x16_bf16 v[80:95], v[152:155], v[136:139], v[80:95]
	ds_read_b64_tr_b16 v[244:245], v177 offset:0xce00
	ds_read_b64_tr_b16 v[246:247], v177 offset:0xde00
	s_waitcnt lgkmcnt(6)
	v_mfma_f32_32x32x16_bf16 v[80:95], v[156:159], v[140:143], v[80:95]
	ds_read_b64_tr_b16 v[248:249], v177 offset:0xee00
	ds_read_b64_tr_b16 v[250:251], v177 offset:0xfe00
	s_waitcnt lgkmcnt(6)
	v_mfma_f32_32x32x16_bf16 v[96:111], v[236:239], v[128:131], v[96:111]
	s_waitcnt lgkmcnt(4)
	v_mfma_f32_32x32x16_bf16 v[96:111], v[240:243], v[132:135], v[96:111]
	s_waitcnt lgkmcnt(2)
	v_mfma_f32_32x32x16_bf16 v[96:111], v[244:247], v[136:139], v[96:111]
	s_waitcnt lgkmcnt(0)
	v_mfma_f32_32x32x16_bf16 v[96:111], v[248:251], v[140:143], v[96:111]
	ds_read_b128 v[128:131], v182 offset:0
	ds_read_b128 v[132:135], v182 offset:0x2000
	ds_read_b128 v[136:139], v181 offset:0
	ds_read_b128 v[236:239], v183 offset:0
	ds_read_b128 v[240:243], v183 offset:0x2000
	ds_read_b128 v[244:247], v181 offset:0x400
	s_waitcnt lgkmcnt(3)
	s_nop 0
	v_mfma_f32_32x32x16_bf16 v[144:159], v[128:131], v[136:139], 0
	v_mfma_f32_32x32x16_bf16 v[128:143], v[132:135], v[136:139], 0
	ds_read_b128 v[248:251], v184 offset:0
	ds_read_b128 v[194:197], v184 offset:0x2000
	ds_read_b128 v[222:225], v181 offset:0x800
	s_waitcnt lgkmcnt(3)
	v_mfma_f32_32x32x16_bf16 v[144:159], v[236:239], v[244:247], v[144:159]
	v_mfma_f32_32x32x16_bf16 v[128:143], v[240:243], v[244:247], v[128:143]
	ds_read_b128 v[236:239], v185 offset:0
	ds_read_b128 v[240:243], v185 offset:0x2000
	ds_read_b128 v[244:247], v181 offset:0xc00
	s_waitcnt lgkmcnt(3)
	v_mfma_f32_32x32x16_bf16 v[144:159], v[248:251], v[222:225], v[144:159]
	v_mfma_f32_32x32x16_bf16 v[128:143], v[194:197], v[222:225], v[128:143]
	ds_read_b128 v[194:197], v182 offset:0x80
	ds_read_b128 v[222:225], v182 offset:0x2080
	ds_read_b128 v[248:251], v181 offset:0x1000
	s_waitcnt lgkmcnt(3)
	v_mfma_f32_32x32x16_bf16 v[144:159], v[236:239], v[244:247], v[144:159]
	v_mfma_f32_32x32x16_bf16 v[128:143], v[240:243], v[244:247], v[128:143]
	ds_read_b128 v[236:239], v183 offset:0x80
	ds_read_b128 v[240:243], v183 offset:0x2080
	ds_read_b128 v[244:247], v181 offset:0x1400
	s_waitcnt lgkmcnt(3)
	v_mfma_f32_32x32x16_bf16 v[144:159], v[194:197], v[248:251], v[144:159]
	v_mfma_f32_32x32x16_bf16 v[128:143], v[222:225], v[248:251], v[128:143]
	ds_read_b128 v[194:197], v184 offset:0x80
	ds_read_b128 v[222:225], v184 offset:0x2080
	ds_read_b128 v[248:251], v181 offset:0x1800
	s_waitcnt lgkmcnt(3)
	v_mfma_f32_32x32x16_bf16 v[144:159], v[236:239], v[244:247], v[144:159]
	v_mfma_f32_32x32x16_bf16 v[128:143], v[240:243], v[244:247], v[128:143]
	ds_read_b128 v[236:239], v185 offset:0x80
	ds_read_b128 v[240:243], v185 offset:0x2080
	s_waitcnt lgkmcnt(2)
	v_mfma_f32_32x32x16_bf16 v[144:159], v[194:197], v[248:251], v[144:159]
	v_mfma_f32_32x32x16_bf16 v[128:143], v[222:225], v[248:251], v[128:143]
	s_waitcnt lgkmcnt(0)
	v_mfma_f32_32x32x16_bf16 v[144:159], v[236:239], v[166:169], v[144:159]
	v_mfma_f32_32x32x16_bf16 v[128:143], v[240:243], v[166:169], v[128:143]
	s_bitcmp0_b32 s100, 8
	s_cbranch_scc1 .Lstg_a3
	s_waitcnt vmcnt(0)
	s_waitcnt lgkmcnt(0)
	s_barrier
	s_sleep 7

.LBB0_539:
	ds_read_b64_tr_b16 v[144:145], v177 offset:0
	ds_read_b64_tr_b16 v[146:147], v177 offset:0x1000
	ds_read_b64_tr_b16 v[148:149], v177 offset:0x2000
	ds_read_b64_tr_b16 v[150:151], v177 offset:0x3000
	ds_read_b64_tr_b16 v[152:153], v177 offset:0x4000
	ds_read_b64_tr_b16 v[154:155], v177 offset:0x5000
	ds_read_b64_tr_b16 v[156:157], v177 offset:0x6000
	ds_read_b64_tr_b16 v[158:159], v177 offset:0x7000
	s_waitcnt lgkmcnt(6)
	s_nop 0
	v_mfma_f32_32x32x16_bf16 v[112:127], v[144:147], v[128:131], v[112:127]
	ds_read_b64_tr_b16 v[170:171], v177 offset:0x200
	ds_read_b64_tr_b16 v[172:173], v177 offset:0x1200
	s_waitcnt lgkmcnt(6)
	v_mfma_f32_32x32x16_bf16 v[112:127], v[148:151], v[132:135], v[112:127]
	ds_read_b64_tr_b16 v[182:183], v177 offset:0x2200
	ds_read_b64_tr_b16 v[184:185], v177 offset:0x3200
	s_waitcnt lgkmcnt(6)
	v_mfma_f32_32x32x16_bf16 v[112:127], v[152:155], v[136:139], v[112:127]
	ds_read_b64_tr_b16 v[190:191], v177 offset:0x4200
	ds_read_b64_tr_b16 v[192:193], v177 offset:0x5200
	s_waitcnt lgkmcnt(6)
	v_mfma_f32_32x32x16_bf16 v[112:127], v[156:159], v[140:143], v[112:127]
	ds_read_b64_tr_b16 v[198:199], v177 offset:0x6200
	ds_read_b64_tr_b16 v[200:201], v177 offset:0x7200
	s_waitcnt lgkmcnt(6)
	v_mfma_f32_32x32x16_bf16 v[0:15], v[170:173], v[128:131], v[0:15]
	ds_read_b64_tr_b16 v[144:145], v177 offset:0x400
	ds_read_b64_tr_b16 v[146:147], v177 offset:0x1400
	s_waitcnt lgkmcnt(6)
	v_mfma_f32_32x32x16_bf16 v[0:15], v[182:185], v[132:135], v[0:15]
	ds_read_b64_tr_b16 v[148:149], v177 offset:0x2400
	ds_read_b64_tr_b16 v[150:151], v177 offset:0x3400
	s_waitcnt lgkmcnt(6)
	v_mfma_f32_32x32x16_bf16 v[0:15], v[190:193], v[136:139], v[0:15]
	ds_read_b64_tr_b16 v[152:153], v177 offset:0x4400
	ds_read_b64_tr_b16 v[154:155], v177 offset:0x5400
	s_waitcnt lgkmcnt(6)
	v_mfma_f32_32x32x16_bf16 v[0:15], v[198:201], v[140:143], v[0:15]
	ds_read_b64_tr_b16 v[156:157], v177 offset:0x6400
	ds_read_b64_tr_b16 v[158:159], v177 offset:0x7400
	s_waitcnt lgkmcnt(6)
	v_mfma_f32_32x32x16_bf16 v[16:31], v[144:147], v[128:131], v[16:31]
	ds_read_b64_tr_b16 v[170:171], v177 offset:0x600
	ds_read_b64_tr_b16 v[172:173], v177 offset:0x1600
	s_waitcnt lgkmcnt(6)
	v_mfma_f32_32x32x16_bf16 v[16:31], v[148:151], v[132:135], v[16:31]
	ds_read_b64_tr_b16 v[182:183], v177 offset:0x2600
	ds_read_b64_tr_b16 v[184:185], v177 offset:0x3600
	s_waitcnt lgkmcnt(6)
	v_mfma_f32_32x32x16_bf16 v[16:31], v[152:155], v[136:139], v[16:31]
	ds_read_b64_tr_b16 v[190:191], v177 offset:0x4600
	ds_read_b64_tr_b16 v[192:193], v177 offset:0x5600
	s_waitcnt lgkmcnt(6)
	v_mfma_f32_32x32x16_bf16 v[16:31], v[156:159], v[140:143], v[16:31]
	ds_read_b64_tr_b16 v[198:199], v177 offset:0x6600
	ds_read_b64_tr_b16 v[200:201], v177 offset:0x7600
	s_waitcnt lgkmcnt(6)
	v_mfma_f32_32x32x16_bf16 v[32:47], v[170:173], v[128:131], v[32:47]
	ds_read_b64_tr_b16 v[144:145], v177 offset:0x800
	ds_read_b64_tr_b16 v[146:147], v177 offset:0x1800
	s_waitcnt lgkmcnt(6)
	v_mfma_f32_32x32x16_bf16 v[32:47], v[182:185], v[132:135], v[32:47]
	ds_read_b64_tr_b16 v[148:149], v177 offset:0x2800
	ds_read_b64_tr_b16 v[150:151], v177 offset:0x3800
	s_waitcnt lgkmcnt(6)
	v_mfma_f32_32x32x16_bf16 v[32:47], v[190:193], v[136:139], v[32:47]
	ds_read_b64_tr_b16 v[152:153], v177 offset:0x4800
	ds_read_b64_tr_b16 v[154:155], v177 offset:0x5800
	s_waitcnt lgkmcnt(6)
	v_mfma_f32_32x32x16_bf16 v[32:47], v[198:201], v[140:143], v[32:47]
	ds_read_b64_tr_b16 v[156:157], v177 offset:0x6800
	ds_read_b64_tr_b16 v[158:159], v177 offset:0x7800
	s_waitcnt lgkmcnt(6)
	v_mfma_f32_32x32x16_bf16 v[48:63], v[144:147], v[128:131], v[48:63]
	ds_read_b64_tr_b16 v[170:171], v177 offset:0xa00
	ds_read_b64_tr_b16 v[172:173], v177 offset:0x1a00
	s_waitcnt lgkmcnt(6)
	v_mfma_f32_32x32x16_bf16 v[48:63], v[148:151], v[132:135], v[48:63]
	ds_read_b64_tr_b16 v[182:183], v177 offset:0x2a00
	ds_read_b64_tr_b16 v[184:185], v177 offset:0x3a00
	s_waitcnt lgkmcnt(6)
	v_mfma_f32_32x32x16_bf16 v[48:63], v[152:155], v[136:139], v[48:63]
	ds_read_b64_tr_b16 v[190:191], v177 offset:0x4a00
	ds_read_b64_tr_b16 v[192:193], v177 offset:0x5a00
	s_waitcnt lgkmcnt(6)
	v_mfma_f32_32x32x16_bf16 v[48:63], v[156:159], v[140:143], v[48:63]
	ds_read_b64_tr_b16 v[198:199], v177 offset:0x6a00
	ds_read_b64_tr_b16 v[200:201], v177 offset:0x7a00
	s_waitcnt lgkmcnt(6)
	v_mfma_f32_32x32x16_bf16 v[64:79], v[170:173], v[128:131], v[64:79]
	ds_read_b64_tr_b16 v[144:145], v177 offset:0xc00
	ds_read_b64_tr_b16 v[146:147], v177 offset:0x1c00
	s_waitcnt lgkmcnt(6)
	v_mfma_f32_32x32x16_bf16 v[64:79], v[182:185], v[132:135], v[64:79]
	ds_read_b64_tr_b16 v[148:149], v177 offset:0x2c00
	ds_read_b64_tr_b16 v[150:151], v177 offset:0x3c00
	s_waitcnt lgkmcnt(6)
	v_mfma_f32_32x32x16_bf16 v[64:79], v[190:193], v[136:139], v[64:79]
	ds_read_b64_tr_b16 v[152:153], v177 offset:0x4c00
	ds_read_b64_tr_b16 v[154:155], v177 offset:0x5c00
	s_waitcnt lgkmcnt(6)
	v_mfma_f32_32x32x16_bf16 v[64:79], v[198:201], v[140:143], v[64:79]
	ds_read_b64_tr_b16 v[156:157], v177 offset:0x6c00
	ds_read_b64_tr_b16 v[158:159], v177 offset:0x7c00
	s_waitcnt lgkmcnt(6)
	v_mfma_f32_32x32x16_bf16 v[80:95], v[144:147], v[128:131], v[80:95]
	ds_read_b64_tr_b16 v[170:171], v177 offset:0xe00
	ds_read_b64_tr_b16 v[172:173], v177 offset:0x1e00
	s_waitcnt lgkmcnt(6)
	v_mfma_f32_32x32x16_bf16 v[80:95], v[148:151], v[132:135], v[80:95]
	ds_read_b64_tr_b16 v[182:183], v177 offset:0x2e00
	ds_read_b64_tr_b16 v[184:185], v177 offset:0x3e00
	s_waitcnt lgkmcnt(6)
	v_mfma_f32_32x32x16_bf16 v[80:95], v[152:155], v[136:139], v[80:95]
	ds_read_b64_tr_b16 v[190:191], v177 offset:0x4e00
	ds_read_b64_tr_b16 v[192:193], v177 offset:0x5e00
	s_waitcnt lgkmcnt(6)
	v_mfma_f32_32x32x16_bf16 v[80:95], v[156:159], v[140:143], v[80:95]
	ds_read_b64_tr_b16 v[198:199], v177 offset:0x6e00
	ds_read_b64_tr_b16 v[200:201], v177 offset:0x7e00
	s_waitcnt lgkmcnt(6)
	v_mfma_f32_32x32x16_bf16 v[96:111], v[170:173], v[128:131], v[96:111]
	s_waitcnt lgkmcnt(4)
	v_mfma_f32_32x32x16_bf16 v[96:111], v[182:185], v[132:135], v[96:111]
	s_waitcnt lgkmcnt(2)
	v_mfma_f32_32x32x16_bf16 v[96:111], v[190:193], v[136:139], v[96:111]
	s_waitcnt lgkmcnt(0)
	v_mfma_f32_32x32x16_bf16 v[96:111], v[198:201], v[140:143], v[96:111]
	ds_read_b128 v[128:131], v189 offset:0
	ds_read_b128 v[132:135], v189 offset:0x2000
	ds_read_b128 v[136:139], v181 offset:0
	ds_read_b128 v[170:173], v188 offset:0
	ds_read_b128 v[182:185], v188 offset:0x2000
	ds_read_b128 v[190:193], v181 offset:0x400
	s_waitcnt lgkmcnt(3)
	s_nop 0
	v_mfma_f32_32x32x16_bf16 v[144:159], v[128:131], v[136:139], 0
	v_mfma_f32_32x32x16_bf16 v[128:143], v[132:135], v[136:139], 0
	ds_read_b128 v[198:201], v187 offset:0
	ds_read_b128 v[202:205], v187 offset:0x2000
	ds_read_b128 v[206:209], v181 offset:0x800
	s_waitcnt lgkmcnt(3)
	v_mfma_f32_32x32x16_bf16 v[144:159], v[170:173], v[190:193], v[144:159]
	v_mfma_f32_32x32x16_bf16 v[128:143], v[182:185], v[190:193], v[128:143]
	ds_read_b128 v[170:173], v186 offset:0
	ds_read_b128 v[182:185], v186 offset:0x2000
	ds_read_b128 v[190:193], v181 offset:0xc00
	s_waitcnt lgkmcnt(3)
	v_mfma_f32_32x32x16_bf16 v[144:159], v[198:201], v[206:209], v[144:159]
	v_mfma_f32_32x32x16_bf16 v[128:143], v[202:205], v[206:209], v[128:143]
	ds_read_b128 v[198:201], v189 offset:0x80
	ds_read_b128 v[202:205], v189 offset:0x2080
	ds_read_b128 v[206:209], v181 offset:0x1000
	s_waitcnt lgkmcnt(3)
	v_mfma_f32_32x32x16_bf16 v[144:159], v[170:173], v[190:193], v[144:159]
	v_mfma_f32_32x32x16_bf16 v[128:143], v[182:185], v[190:193], v[128:143]
	ds_read_b128 v[170:173], v188 offset:0x80
	ds_read_b128 v[182:185], v188 offset:0x2080
	ds_read_b128 v[188:191], v181 offset:0x1400
	s_waitcnt lgkmcnt(3)
	v_mfma_f32_32x32x16_bf16 v[144:159], v[198:201], v[206:209], v[144:159]
	v_mfma_f32_32x32x16_bf16 v[128:143], v[202:205], v[206:209], v[128:143]
	ds_read_b128 v[198:201], v187 offset:0x80
	ds_read_b128 v[202:205], v187 offset:0x2080
	ds_read_b128 v[206:209], v181 offset:0x1800
	s_waitcnt lgkmcnt(3)
	v_mfma_f32_32x32x16_bf16 v[144:159], v[170:173], v[188:191], v[144:159]
	v_mfma_f32_32x32x16_bf16 v[128:143], v[182:185], v[188:191], v[128:143]
	ds_read_b128 v[170:173], v186 offset:0x80
	ds_read_b128 v[182:185], v186 offset:0x2080
	s_waitcnt lgkmcnt(2)
	v_mfma_f32_32x32x16_bf16 v[144:159], v[198:201], v[206:209], v[144:159]
	v_mfma_f32_32x32x16_bf16 v[128:143], v[202:205], v[206:209], v[128:143]
	s_waitcnt lgkmcnt(0)
	v_mfma_f32_32x32x16_bf16 v[144:159], v[170:173], v[166:169], v[144:159]
	v_mfma_f32_32x32x16_bf16 v[128:143], v[182:185], v[166:169], v[128:143]
	s_bitcmp0_b32 s100, 8
	s_cbranch_scc1 .Lstg_a4
	s_waitcnt vmcnt(0)
	s_waitcnt lgkmcnt(0)
	s_barrier
	s_sleep 7

.LBB0_554:
	s_or_b64 exec, exec, s[4:5]
	s_ashr_i32 s95, s94, 31
	s_add_u32 s4, s2, s16
	s_addc_u32 s3, s3, 0
	v_mov_b32_e32 v38, v165
	s_add_u32 s2, s4, 0x2800
	s_addc_u32 s33, s3, 0
	v_readfirstlane_b32 s5, v38
	s_ashr_i32 s79, s5, 6
	v_bfe_u32 v0, v38, 5, 1
	v_and_b32_e32 v175, 31, v38
	s_lshl_b32 s92, s79, 5
	v_lshlrev_b32_e32 v32, 2, v0
	s_add_i32 s82, s92, s78
	v_sub_u32_e32 v1, v175, v32
	v_lshlrev_b32_e32 v176, 4, v0
	s_lshl_b32 s76, s79, 3
	v_bfe_u32 v0, v38, 4, 2
	v_writelane_b32 v255, s16, 17
	v_add_u32_e32 v179, s82, v1
	v_or_b32_e32 v1, s76, v0
	v_and_b32_e32 v2, 15, v38
	s_lshl_b32 s5, s79, 12
	v_and_b32_e32 v39, 63, v38
	v_bitop3_b32 v3, v0, v38, 15 bitop3:0x78
	v_mul_lo_u32 v1, v1, s84
	v_bitop3_b32 v0, v0, v2, 4 bitop3:0x36
	s_add_i32 s93, s5, s77
	s_mul_i32 s5, s79, 0x1c00
	v_readlane_b32 s7, v255, 51
	s_waitcnt vmcnt(16)
	v_lshlrev_b32_e32 v40, 4, v39
	v_lshl_or_b32 v0, v0, 4, v1
	s_lshl_b32 s83, s79, 11
	v_readlane_b32 s6, v255, 53
	s_add_i32 s5, s7, s5
	v_lshl_or_b32 v160, v3, 4, v1
	v_add_u32_e32 v170, 0x1a000, v0
	s_add_i32 s83, s83, s6
	v_add_u32_e32 v180, s5, v40
	s_waitcnt vmcnt(16) lgkmcnt(0)
	v_mov_b64_e32 v[218:219], v[128:129]
	v_mov_b64_e32 v[220:221], v[130:131]
	v_mov_b64_e32 v[222:223], v[132:133]
	v_mov_b64_e32 v[224:225], v[134:135]
	v_mov_b64_e32 v[230:231], v[136:137]
	v_mov_b64_e32 v[232:233], v[138:139]
	v_mov_b64_e32 v[234:235], v[140:141]
	v_mov_b64_e32 v[236:237], v[142:143]
	v_mov_b64_e32 v[238:239], v[144:145]
	v_mov_b64_e32 v[240:241], v[146:147]
	v_mov_b64_e32 v[242:243], v[148:149]
	v_mov_b64_e32 v[244:245], v[150:151]
	v_mov_b64_e32 v[246:247], v[152:153]
	v_mov_b64_e32 v[248:249], v[154:155]
	s_add_u32 s4, s4, 0x1a2800
	s_addc_u32 s5, s3, 0
	v_lshl_add_u64 v[0:1], s[4:5], 0, v[160:161]
	s_add_i32 s84, s83, 0x4000
	s_mov_b32 s3, m0
	s_mov_b32 m0, s84
	s_nop 0
	global_load_lds_dwordx4 v[0:1], off
	s_mov_b32 m0, s3
	v_mov_b32_e32 v171, v161
	v_lshl_add_u64 v[0:1], s[4:5], 0, v[170:171]
	s_add_i32 s85, s83, 0x4400
	s_mov_b32 s3, m0
	s_mov_b32 m0, s85
	s_nop 0
	global_load_lds_dwordx4 v[0:1], off
	s_mov_b32 m0, s3
	s_waitcnt lgkmcnt(0)
	s_barrier
	v_lshlrev_b32_e32 v0, 4, v38
	s_movk_i32 s3, 0x70
	v_lshlrev_b32_e32 v33, 8, v175
	v_and_b32_e32 v1, 0x70, v0
	v_bitop3_b32 v34, v176, v0, s3 bitop3:0x78
	s_movk_i32 s3, 0x60
	v_add_u32_e32 v2, s6, v33
	v_bitop3_b32 v35, v176, v1, 32 bitop3:0x36
	v_bitop3_b32 v36, v176, v1, 64 bitop3:0x36
	v_bitop3_b32 v37, v176, v1, s3 bitop3:0x36
	v_add_u32_e32 v181, v34, v2
	v_add_u32_e32 v182, v35, v2
	v_add_u32_e32 v183, v36, v2
	v_add_u32_e32 v184, v37, v2
	ds_read_b128 v[0:3], v181 offset:0
	ds_read_b128 v[4:7], v181 offset:0x2000
	ds_read_b128 v[42:45], v182 offset:0
	ds_read_b128 v[46:49], v182 offset:0x2000
	s_waitcnt lgkmcnt(2)
	s_nop 0
	v_mfma_f32_32x32x16_bf16 v[16:31], v[0:3], v[218:221], 0
	v_mfma_f32_32x32x16_bf16 v[0:15], v[4:7], v[218:221], 0
	ds_read_b128 v[54:57], v183 offset:0
	ds_read_b128 v[58:61], v183 offset:0x2000
	s_waitcnt lgkmcnt(2)
	v_mfma_f32_32x32x16_bf16 v[16:31], v[42:45], v[222:225], v[16:31]
	v_mfma_f32_32x32x16_bf16 v[0:15], v[46:49], v[222:225], v[0:15]
	ds_read_b128 v[42:45], v184 offset:0
	ds_read_b128 v[46:49], v184 offset:0x2000
	s_waitcnt lgkmcnt(2)
	v_mfma_f32_32x32x16_bf16 v[16:31], v[54:57], v[230:233], v[16:31]
	v_mfma_f32_32x32x16_bf16 v[0:15], v[58:61], v[230:233], v[0:15]
	ds_read_b128 v[54:57], v181 offset:0x80
	ds_read_b128 v[58:61], v181 offset:0x2080
	s_waitcnt lgkmcnt(2)
	v_mfma_f32_32x32x16_bf16 v[16:31], v[42:45], v[234:237], v[16:31]
	v_mfma_f32_32x32x16_bf16 v[0:15], v[46:49], v[234:237], v[0:15]
	ds_read_b128 v[42:45], v182 offset:0x80
	ds_read_b128 v[46:49], v182 offset:0x2080
	s_waitcnt lgkmcnt(2)
	v_mfma_f32_32x32x16_bf16 v[16:31], v[54:57], v[238:241], v[16:31]
	v_mfma_f32_32x32x16_bf16 v[0:15], v[58:61], v[238:241], v[0:15]
	ds_read_b128 v[54:57], v183 offset:0x80
	ds_read_b128 v[58:61], v183 offset:0x2080
	s_waitcnt lgkmcnt(2)
	v_mfma_f32_32x32x16_bf16 v[16:31], v[42:45], v[242:245], v[16:31]
	v_mfma_f32_32x32x16_bf16 v[0:15], v[46:49], v[242:245], v[0:15]
	ds_read_b128 v[42:45], v184 offset:0x80
	ds_read_b128 v[46:49], v184 offset:0x2080
	s_waitcnt lgkmcnt(2)
	v_mfma_f32_32x32x16_bf16 v[16:31], v[54:57], v[246:249], v[16:31]
	v_mfma_f32_32x32x16_bf16 v[0:15], v[58:61], v[246:249], v[0:15]
	s_waitcnt lgkmcnt(0)
	v_mfma_f32_32x32x16_bf16 v[16:31], v[42:45], v[166:169], v[16:31]
	v_mfma_f32_32x32x16_bf16 v[0:15], v[46:49], v[166:169], v[0:15]
	s_bitcmp0_b32 s100, 8
	s_cbranch_scc1 .Lstg_a9
	s_waitcnt vmcnt(0)
	s_waitcnt lgkmcnt(0)
	s_barrier
	s_sleep 7

.LBB0_557:
	ds_read_b64_tr_b16 v[144:145], v177 offset:0
	ds_read_b64_tr_b16 v[146:147], v177 offset:0x1000
	ds_read_b64_tr_b16 v[148:149], v177 offset:0x2000
	ds_read_b64_tr_b16 v[150:151], v177 offset:0x3000
	ds_read_b64_tr_b16 v[152:153], v177 offset:0x4000
	ds_read_b64_tr_b16 v[154:155], v177 offset:0x5000
	ds_read_b64_tr_b16 v[156:157], v177 offset:0x6000
	ds_read_b64_tr_b16 v[158:159], v177 offset:0x7000
	s_waitcnt lgkmcnt(6)
	s_nop 0
	v_mfma_f32_32x32x16_bf16 v[112:127], v[144:147], v[128:131], v[112:127]
	ds_read_b64_tr_b16 v[192:193], v177 offset:0x200
	ds_read_b64_tr_b16 v[194:195], v177 offset:0x1200
	s_waitcnt lgkmcnt(6)
	v_mfma_f32_32x32x16_bf16 v[112:127], v[148:151], v[132:135], v[112:127]
	ds_read_b64_tr_b16 v[196:197], v177 offset:0x2200
	ds_read_b64_tr_b16 v[198:199], v177 offset:0x3200
	s_waitcnt lgkmcnt(6)
	v_mfma_f32_32x32x16_bf16 v[112:127], v[152:155], v[136:139], v[112:127]
	ds_read_b64_tr_b16 v[200:201], v177 offset:0x4200
	ds_read_b64_tr_b16 v[202:203], v177 offset:0x5200
	s_waitcnt lgkmcnt(6)
	v_mfma_f32_32x32x16_bf16 v[112:127], v[156:159], v[140:143], v[112:127]
	ds_read_b64_tr_b16 v[204:205], v177 offset:0x6200
	ds_read_b64_tr_b16 v[206:207], v177 offset:0x7200
	s_waitcnt lgkmcnt(6)
	v_mfma_f32_32x32x16_bf16 v[80:95], v[192:195], v[128:131], v[80:95]
	ds_read_b64_tr_b16 v[144:145], v177 offset:0x400
	ds_read_b64_tr_b16 v[146:147], v177 offset:0x1400
	s_waitcnt lgkmcnt(6)
	v_mfma_f32_32x32x16_bf16 v[80:95], v[196:199], v[132:135], v[80:95]
	ds_read_b64_tr_b16 v[148:149], v177 offset:0x2400
	ds_read_b64_tr_b16 v[150:151], v177 offset:0x3400
	s_waitcnt lgkmcnt(6)
	v_mfma_f32_32x32x16_bf16 v[80:95], v[200:203], v[136:139], v[80:95]
	ds_read_b64_tr_b16 v[152:153], v177 offset:0x4400
	ds_read_b64_tr_b16 v[154:155], v177 offset:0x5400
	s_waitcnt lgkmcnt(6)
	v_mfma_f32_32x32x16_bf16 v[80:95], v[204:207], v[140:143], v[80:95]
	ds_read_b64_tr_b16 v[156:157], v177 offset:0x6400
	ds_read_b64_tr_b16 v[158:159], v177 offset:0x7400
	s_waitcnt lgkmcnt(6)
	v_mfma_f32_32x32x16_bf16 v[96:111], v[144:147], v[128:131], v[96:111]
	ds_read_b64_tr_b16 v[192:193], v177 offset:0x600
	ds_read_b64_tr_b16 v[194:195], v177 offset:0x1600
	s_waitcnt lgkmcnt(6)
	v_mfma_f32_32x32x16_bf16 v[96:111], v[148:151], v[132:135], v[96:111]
	ds_read_b64_tr_b16 v[196:197], v177 offset:0x2600
	ds_read_b64_tr_b16 v[198:199], v177 offset:0x3600
	s_waitcnt lgkmcnt(6)
	v_mfma_f32_32x32x16_bf16 v[96:111], v[152:155], v[136:139], v[96:111]
	ds_read_b64_tr_b16 v[200:201], v177 offset:0x4600
	ds_read_b64_tr_b16 v[202:203], v177 offset:0x5600
	s_waitcnt lgkmcnt(6)
	v_mfma_f32_32x32x16_bf16 v[96:111], v[156:159], v[140:143], v[96:111]
	ds_read_b64_tr_b16 v[204:205], v177 offset:0x6600
	ds_read_b64_tr_b16 v[206:207], v177 offset:0x7600
	s_waitcnt lgkmcnt(6)
	v_mfma_f32_32x32x16_bf16 v[64:79], v[192:195], v[128:131], v[64:79]
	ds_read_b64_tr_b16 v[144:145], v177 offset:0x800
	ds_read_b64_tr_b16 v[146:147], v177 offset:0x1800
	s_waitcnt lgkmcnt(6)
	v_mfma_f32_32x32x16_bf16 v[64:79], v[196:199], v[132:135], v[64:79]
	ds_read_b64_tr_b16 v[148:149], v177 offset:0x2800
	ds_read_b64_tr_b16 v[150:151], v177 offset:0x3800
	s_waitcnt lgkmcnt(6)
	v_mfma_f32_32x32x16_bf16 v[64:79], v[200:203], v[136:139], v[64:79]
	ds_read_b64_tr_b16 v[152:153], v177 offset:0x4800
	ds_read_b64_tr_b16 v[154:155], v177 offset:0x5800
	s_waitcnt lgkmcnt(6)
	v_mfma_f32_32x32x16_bf16 v[64:79], v[204:207], v[140:143], v[64:79]
	ds_read_b64_tr_b16 v[156:157], v177 offset:0x6800
	ds_read_b64_tr_b16 v[158:159], v177 offset:0x7800
	s_waitcnt lgkmcnt(6)
	v_mfma_f32_32x32x16_bf16 v[48:63], v[144:147], v[128:131], v[48:63]
	ds_read_b64_tr_b16 v[192:193], v177 offset:0xa00
	ds_read_b64_tr_b16 v[194:195], v177 offset:0x1a00
	s_waitcnt lgkmcnt(6)
	v_mfma_f32_32x32x16_bf16 v[48:63], v[148:151], v[132:135], v[48:63]
	ds_read_b64_tr_b16 v[196:197], v177 offset:0x2a00
	ds_read_b64_tr_b16 v[198:199], v177 offset:0x3a00
	s_waitcnt lgkmcnt(6)
	v_mfma_f32_32x32x16_bf16 v[48:63], v[152:155], v[136:139], v[48:63]
	ds_read_b64_tr_b16 v[200:201], v177 offset:0x4a00
	ds_read_b64_tr_b16 v[202:203], v177 offset:0x5a00
	s_waitcnt lgkmcnt(6)
	v_mfma_f32_32x32x16_bf16 v[48:63], v[156:159], v[140:143], v[48:63]
	ds_read_b64_tr_b16 v[204:205], v177 offset:0x6a00
	ds_read_b64_tr_b16 v[206:207], v177 offset:0x7a00
	s_waitcnt lgkmcnt(6)
	v_mfma_f32_32x32x16_bf16 v[32:47], v[192:195], v[128:131], v[32:47]
	ds_read_b64_tr_b16 v[144:145], v177 offset:0xc00
	ds_read_b64_tr_b16 v[146:147], v177 offset:0x1c00
	s_waitcnt lgkmcnt(6)
	v_mfma_f32_32x32x16_bf16 v[32:47], v[196:199], v[132:135], v[32:47]
	ds_read_b64_tr_b16 v[148:149], v177 offset:0x2c00
	ds_read_b64_tr_b16 v[150:151], v177 offset:0x3c00
	s_waitcnt lgkmcnt(6)
	v_mfma_f32_32x32x16_bf16 v[32:47], v[200:203], v[136:139], v[32:47]
	ds_read_b64_tr_b16 v[152:153], v177 offset:0x4c00
	ds_read_b64_tr_b16 v[154:155], v177 offset:0x5c00
	s_waitcnt lgkmcnt(6)
	v_mfma_f32_32x32x16_bf16 v[32:47], v[204:207], v[140:143], v[32:47]
	ds_read_b64_tr_b16 v[156:157], v177 offset:0x6c00
	ds_read_b64_tr_b16 v[158:159], v177 offset:0x7c00
	s_waitcnt lgkmcnt(6)
	v_mfma_f32_32x32x16_bf16 v[16:31], v[144:147], v[128:131], v[16:31]
	ds_read_b64_tr_b16 v[192:193], v177 offset:0xe00
	ds_read_b64_tr_b16 v[194:195], v177 offset:0x1e00
	s_waitcnt lgkmcnt(6)
	v_mfma_f32_32x32x16_bf16 v[16:31], v[148:151], v[132:135], v[16:31]
	ds_read_b64_tr_b16 v[196:197], v177 offset:0x2e00
	ds_read_b64_tr_b16 v[198:199], v177 offset:0x3e00
	s_waitcnt lgkmcnt(6)
	v_mfma_f32_32x32x16_bf16 v[16:31], v[152:155], v[136:139], v[16:31]
	ds_read_b64_tr_b16 v[200:201], v177 offset:0x4e00
	ds_read_b64_tr_b16 v[202:203], v177 offset:0x5e00
	s_waitcnt lgkmcnt(6)
	v_mfma_f32_32x32x16_bf16 v[16:31], v[156:159], v[140:143], v[16:31]
	ds_read_b64_tr_b16 v[204:205], v177 offset:0x6e00
	ds_read_b64_tr_b16 v[206:207], v177 offset:0x7e00
	s_waitcnt lgkmcnt(6)
	v_mfma_f32_32x32x16_bf16 v[0:15], v[192:195], v[128:131], v[0:15]
	s_waitcnt lgkmcnt(4)
	v_mfma_f32_32x32x16_bf16 v[0:15], v[196:199], v[132:135], v[0:15]
	s_waitcnt lgkmcnt(2)
	v_mfma_f32_32x32x16_bf16 v[0:15], v[200:203], v[136:139], v[0:15]
	s_waitcnt lgkmcnt(0)
	v_mfma_f32_32x32x16_bf16 v[0:15], v[204:207], v[140:143], v[0:15]
	ds_read_b128 v[128:131], v188 offset:0
	ds_read_b128 v[132:135], v188 offset:0x2000
	ds_read_b128 v[192:195], v187 offset:0
	ds_read_b128 v[196:199], v187 offset:0x2000
	s_waitcnt lgkmcnt(2)
	s_nop 0
	v_mfma_f32_32x32x16_bf16 v[144:159], v[128:131], v[218:221], 0
	v_mfma_f32_32x32x16_bf16 v[128:143], v[132:135], v[218:221], 0
	ds_read_b128 v[204:207], v186 offset:0
	ds_read_b128 v[208:211], v186 offset:0x2000
	s_waitcnt lgkmcnt(2)
	v_mfma_f32_32x32x16_bf16 v[144:159], v[192:195], v[222:225], v[144:159]
	v_mfma_f32_32x32x16_bf16 v[128:143], v[196:199], v[222:225], v[128:143]
	ds_read_b128 v[192:195], v185 offset:0
	ds_read_b128 v[196:199], v185 offset:0x2000
	s_waitcnt lgkmcnt(2)
	v_mfma_f32_32x32x16_bf16 v[144:159], v[204:207], v[230:233], v[144:159]
	v_mfma_f32_32x32x16_bf16 v[128:143], v[208:211], v[230:233], v[128:143]
	ds_read_b128 v[204:207], v188 offset:0x80
	ds_read_b128 v[208:211], v188 offset:0x2080
	s_waitcnt lgkmcnt(2)
	v_mfma_f32_32x32x16_bf16 v[144:159], v[192:195], v[234:237], v[144:159]
	v_mfma_f32_32x32x16_bf16 v[128:143], v[196:199], v[234:237], v[128:143]
	ds_read_b128 v[192:195], v187 offset:0x80
	ds_read_b128 v[196:199], v187 offset:0x2080
	s_waitcnt lgkmcnt(2)
	v_mfma_f32_32x32x16_bf16 v[144:159], v[204:207], v[238:241], v[144:159]
	v_mfma_f32_32x32x16_bf16 v[128:143], v[208:211], v[238:241], v[128:143]
	ds_read_b128 v[204:207], v186 offset:0x80
	ds_read_b128 v[208:211], v186 offset:0x2080
	s_waitcnt lgkmcnt(2)
	v_mfma_f32_32x32x16_bf16 v[144:159], v[192:195], v[242:245], v[144:159]
	v_mfma_f32_32x32x16_bf16 v[128:143], v[196:199], v[242:245], v[128:143]
	ds_read_b128 v[192:195], v185 offset:0x80
	ds_read_b128 v[196:199], v185 offset:0x2080
	s_waitcnt lgkmcnt(2)
	v_mfma_f32_32x32x16_bf16 v[144:159], v[204:207], v[246:249], v[144:159]
	v_mfma_f32_32x32x16_bf16 v[128:143], v[208:211], v[246:249], v[128:143]
	s_waitcnt lgkmcnt(0)
	v_mfma_f32_32x32x16_bf16 v[144:159], v[192:195], v[166:169], v[144:159]
	v_mfma_f32_32x32x16_bf16 v[128:143], v[196:199], v[166:169], v[128:143]
	s_bitcmp0_b32 s100, 8
	s_cbranch_scc1 .Lstg_a10
	s_waitcnt vmcnt(0)
	s_waitcnt lgkmcnt(0)
	s_barrier
	s_sleep 7

.LBB0_565:
	ds_read_b64_tr_b16 v[144:145], v177 offset:0x8000
	ds_read_b64_tr_b16 v[146:147], v177 offset:0x9000
	ds_read_b64_tr_b16 v[148:149], v177 offset:0xa000
	ds_read_b64_tr_b16 v[150:151], v177 offset:0xb000
	ds_read_b64_tr_b16 v[152:153], v177 offset:0xc000
	ds_read_b64_tr_b16 v[154:155], v177 offset:0xd000
	ds_read_b64_tr_b16 v[156:157], v177 offset:0xe000
	ds_read_b64_tr_b16 v[158:159], v177 offset:0xf000
	s_waitcnt lgkmcnt(6)
	s_nop 0
	v_mfma_f32_32x32x16_bf16 v[112:127], v[144:147], v[128:131], v[112:127]
	ds_read_b64_tr_b16 v[194:195], v177 offset:0x8200
	ds_read_b64_tr_b16 v[196:197], v177 offset:0x9200
	s_waitcnt lgkmcnt(6)
	v_mfma_f32_32x32x16_bf16 v[112:127], v[148:151], v[132:135], v[112:127]
	ds_read_b64_tr_b16 v[198:199], v177 offset:0xa200
	ds_read_b64_tr_b16 v[200:201], v177 offset:0xb200
	s_waitcnt lgkmcnt(6)
	v_mfma_f32_32x32x16_bf16 v[112:127], v[152:155], v[136:139], v[112:127]
	ds_read_b64_tr_b16 v[202:203], v177 offset:0xc200
	ds_read_b64_tr_b16 v[204:205], v177 offset:0xd200
	s_waitcnt lgkmcnt(6)
	v_mfma_f32_32x32x16_bf16 v[112:127], v[156:159], v[140:143], v[112:127]
	ds_read_b64_tr_b16 v[206:207], v177 offset:0xe200
	ds_read_b64_tr_b16 v[208:209], v177 offset:0xf200
	s_waitcnt lgkmcnt(6)
	v_mfma_f32_32x32x16_bf16 v[80:95], v[194:197], v[128:131], v[80:95]
	ds_read_b64_tr_b16 v[144:145], v177 offset:0x8400
	ds_read_b64_tr_b16 v[146:147], v177 offset:0x9400
	s_waitcnt lgkmcnt(6)
	v_mfma_f32_32x32x16_bf16 v[80:95], v[198:201], v[132:135], v[80:95]
	ds_read_b64_tr_b16 v[148:149], v177 offset:0xa400
	ds_read_b64_tr_b16 v[150:151], v177 offset:0xb400
	s_waitcnt lgkmcnt(6)
	v_mfma_f32_32x32x16_bf16 v[80:95], v[202:205], v[136:139], v[80:95]
	ds_read_b64_tr_b16 v[152:153], v177 offset:0xc400
	ds_read_b64_tr_b16 v[154:155], v177 offset:0xd400
	s_waitcnt lgkmcnt(6)
	v_mfma_f32_32x32x16_bf16 v[80:95], v[206:209], v[140:143], v[80:95]
	ds_read_b64_tr_b16 v[156:157], v177 offset:0xe400
	ds_read_b64_tr_b16 v[158:159], v177 offset:0xf400
	s_waitcnt lgkmcnt(6)
	v_mfma_f32_32x32x16_bf16 v[96:111], v[144:147], v[128:131], v[96:111]
	ds_read_b64_tr_b16 v[194:195], v177 offset:0x8600
	ds_read_b64_tr_b16 v[196:197], v177 offset:0x9600
	s_waitcnt lgkmcnt(6)
	v_mfma_f32_32x32x16_bf16 v[96:111], v[148:151], v[132:135], v[96:111]
	ds_read_b64_tr_b16 v[198:199], v177 offset:0xa600
	ds_read_b64_tr_b16 v[200:201], v177 offset:0xb600
	s_waitcnt lgkmcnt(6)
	v_mfma_f32_32x32x16_bf16 v[96:111], v[152:155], v[136:139], v[96:111]
	ds_read_b64_tr_b16 v[202:203], v177 offset:0xc600
	ds_read_b64_tr_b16 v[204:205], v177 offset:0xd600
	s_waitcnt lgkmcnt(6)
	v_mfma_f32_32x32x16_bf16 v[96:111], v[156:159], v[140:143], v[96:111]
	ds_read_b64_tr_b16 v[206:207], v177 offset:0xe600
	ds_read_b64_tr_b16 v[208:209], v177 offset:0xf600
	s_waitcnt lgkmcnt(6)
	v_mfma_f32_32x32x16_bf16 v[64:79], v[194:197], v[128:131], v[64:79]
	ds_read_b64_tr_b16 v[144:145], v177 offset:0x8800
	ds_read_b64_tr_b16 v[146:147], v177 offset:0x9800
	s_waitcnt lgkmcnt(6)
	v_mfma_f32_32x32x16_bf16 v[64:79], v[198:201], v[132:135], v[64:79]
	ds_read_b64_tr_b16 v[148:149], v177 offset:0xa800
	ds_read_b64_tr_b16 v[150:151], v177 offset:0xb800
	s_waitcnt lgkmcnt(6)
	v_mfma_f32_32x32x16_bf16 v[64:79], v[202:205], v[136:139], v[64:79]
	ds_read_b64_tr_b16 v[152:153], v177 offset:0xc800
	ds_read_b64_tr_b16 v[154:155], v177 offset:0xd800
	s_waitcnt lgkmcnt(6)
	v_mfma_f32_32x32x16_bf16 v[64:79], v[206:209], v[140:143], v[64:79]
	ds_read_b64_tr_b16 v[156:157], v177 offset:0xe800
	ds_read_b64_tr_b16 v[158:159], v177 offset:0xf800
	s_waitcnt lgkmcnt(6)
	v_mfma_f32_32x32x16_bf16 v[48:63], v[144:147], v[128:131], v[48:63]
	ds_read_b64_tr_b16 v[194:195], v177 offset:0x8a00
	ds_read_b64_tr_b16 v[196:197], v177 offset:0x9a00
	s_waitcnt lgkmcnt(6)
	v_mfma_f32_32x32x16_bf16 v[48:63], v[148:151], v[132:135], v[48:63]
	ds_read_b64_tr_b16 v[198:199], v177 offset:0xaa00
	ds_read_b64_tr_b16 v[200:201], v177 offset:0xba00
	s_waitcnt lgkmcnt(6)
	v_mfma_f32_32x32x16_bf16 v[48:63], v[152:155], v[136:139], v[48:63]
	ds_read_b64_tr_b16 v[202:203], v177 offset:0xca00
	ds_read_b64_tr_b16 v[204:205], v177 offset:0xda00
	s_waitcnt lgkmcnt(6)
	v_mfma_f32_32x32x16_bf16 v[48:63], v[156:159], v[140:143], v[48:63]
	ds_read_b64_tr_b16 v[206:207], v177 offset:0xea00
	ds_read_b64_tr_b16 v[208:209], v177 offset:0xfa00
	s_waitcnt lgkmcnt(6)
	v_mfma_f32_32x32x16_bf16 v[32:47], v[194:197], v[128:131], v[32:47]
	ds_read_b64_tr_b16 v[144:145], v177 offset:0x8c00
	ds_read_b64_tr_b16 v[146:147], v177 offset:0x9c00
	s_waitcnt lgkmcnt(6)
	v_mfma_f32_32x32x16_bf16 v[32:47], v[198:201], v[132:135], v[32:47]
	ds_read_b64_tr_b16 v[148:149], v177 offset:0xac00
	ds_read_b64_tr_b16 v[150:151], v177 offset:0xbc00
	s_waitcnt lgkmcnt(6)
	v_mfma_f32_32x32x16_bf16 v[32:47], v[202:205], v[136:139], v[32:47]
	ds_read_b64_tr_b16 v[152:153], v177 offset:0xcc00
	ds_read_b64_tr_b16 v[154:155], v177 offset:0xdc00
	s_waitcnt lgkmcnt(6)
	v_mfma_f32_32x32x16_bf16 v[32:47], v[206:209], v[140:143], v[32:47]
	ds_read_b64_tr_b16 v[156:157], v177 offset:0xec00
	ds_read_b64_tr_b16 v[158:159], v177 offset:0xfc00
	s_waitcnt lgkmcnt(6)
	v_mfma_f32_32x32x16_bf16 v[16:31], v[144:147], v[128:131], v[16:31]
	ds_read_b64_tr_b16 v[194:195], v177 offset:0x8e00
	ds_read_b64_tr_b16 v[196:197], v177 offset:0x9e00
	s_waitcnt lgkmcnt(6)
	v_mfma_f32_32x32x16_bf16 v[16:31], v[148:151], v[132:135], v[16:31]
	ds_read_b64_tr_b16 v[198:199], v177 offset:0xae00
	ds_read_b64_tr_b16 v[200:201], v177 offset:0xbe00
	s_waitcnt lgkmcnt(6)
	v_mfma_f32_32x32x16_bf16 v[16:31], v[152:155], v[136:139], v[16:31]
	ds_read_b64_tr_b16 v[202:203], v177 offset:0xce00
	ds_read_b64_tr_b16 v[204:205], v177 offset:0xde00
	s_waitcnt lgkmcnt(6)
	v_mfma_f32_32x32x16_bf16 v[16:31], v[156:159], v[140:143], v[16:31]
	ds_read_b64_tr_b16 v[206:207], v177 offset:0xee00
	ds_read_b64_tr_b16 v[208:209], v177 offset:0xfe00
	s_waitcnt lgkmcnt(6)
	v_mfma_f32_32x32x16_bf16 v[0:15], v[194:197], v[128:131], v[0:15]
	s_waitcnt lgkmcnt(4)
	v_mfma_f32_32x32x16_bf16 v[0:15], v[198:201], v[132:135], v[0:15]
	s_waitcnt lgkmcnt(2)
	v_mfma_f32_32x32x16_bf16 v[0:15], v[202:205], v[136:139], v[0:15]
	s_waitcnt lgkmcnt(0)
	v_mfma_f32_32x32x16_bf16 v[0:15], v[206:209], v[140:143], v[0:15]
	ds_read_b128 v[128:131], v181 offset:0
	ds_read_b128 v[132:135], v181 offset:0x2000
	ds_read_b128 v[194:197], v182 offset:0
	ds_read_b128 v[198:201], v182 offset:0x2000
	s_waitcnt lgkmcnt(2)
	s_nop 0
	v_mfma_f32_32x32x16_bf16 v[144:159], v[128:131], v[218:221], 0
	v_mfma_f32_32x32x16_bf16 v[128:143], v[132:135], v[218:221], 0
	ds_read_b128 v[206:209], v183 offset:0
	ds_read_b128 v[210:213], v183 offset:0x2000
	s_waitcnt lgkmcnt(2)
	v_mfma_f32_32x32x16_bf16 v[144:159], v[194:197], v[222:225], v[144:159]
	v_mfma_f32_32x32x16_bf16 v[128:143], v[198:201], v[222:225], v[128:143]
	ds_read_b128 v[194:197], v184 offset:0
	ds_read_b128 v[198:201], v184 offset:0x2000
	s_waitcnt lgkmcnt(2)
	v_mfma_f32_32x32x16_bf16 v[144:159], v[206:209], v[230:233], v[144:159]
	v_mfma_f32_32x32x16_bf16 v[128:143], v[210:213], v[230:233], v[128:143]
	ds_read_b128 v[206:209], v181 offset:0x80
	ds_read_b128 v[210:213], v181 offset:0x2080
	s_waitcnt lgkmcnt(2)
	v_mfma_f32_32x32x16_bf16 v[144:159], v[194:197], v[234:237], v[144:159]
	v_mfma_f32_32x32x16_bf16 v[128:143], v[198:201], v[234:237], v[128:143]
	ds_read_b128 v[194:197], v182 offset:0x80
	ds_read_b128 v[198:201], v182 offset:0x2080
	s_waitcnt lgkmcnt(2)
	v_mfma_f32_32x32x16_bf16 v[144:159], v[206:209], v[238:241], v[144:159]
	v_mfma_f32_32x32x16_bf16 v[128:143], v[210:213], v[238:241], v[128:143]
	ds_read_b128 v[206:209], v183 offset:0x80
	ds_read_b128 v[210:213], v183 offset:0x2080
	s_waitcnt lgkmcnt(2)
	v_mfma_f32_32x32x16_bf16 v[144:159], v[194:197], v[242:245], v[144:159]
	v_mfma_f32_32x32x16_bf16 v[128:143], v[198:201], v[242:245], v[128:143]
	ds_read_b128 v[194:197], v184 offset:0x80
	ds_read_b128 v[198:201], v184 offset:0x2080
	s_waitcnt lgkmcnt(2)
	v_mfma_f32_32x32x16_bf16 v[144:159], v[206:209], v[246:249], v[144:159]
	v_mfma_f32_32x32x16_bf16 v[128:143], v[210:213], v[246:249], v[128:143]
	s_waitcnt lgkmcnt(0)
	v_mfma_f32_32x32x16_bf16 v[144:159], v[194:197], v[166:169], v[144:159]
	v_mfma_f32_32x32x16_bf16 v[128:143], v[198:201], v[166:169], v[128:143]
	s_bitcmp0_b32 s100, 8
	s_cbranch_scc1 .Lstg_a11
	s_waitcnt vmcnt(0)
	s_waitcnt lgkmcnt(0)
	s_barrier
	s_sleep 7

.LBB0_580:
	ds_read_b64_tr_b16 v[144:145], v177 offset:0
	ds_read_b64_tr_b16 v[146:147], v177 offset:0x1000
	ds_read_b64_tr_b16 v[148:149], v177 offset:0x2000
	ds_read_b64_tr_b16 v[150:151], v177 offset:0x3000
	ds_read_b64_tr_b16 v[152:153], v177 offset:0x4000
	ds_read_b64_tr_b16 v[154:155], v177 offset:0x5000
	ds_read_b64_tr_b16 v[156:157], v177 offset:0x6000
	ds_read_b64_tr_b16 v[158:159], v177 offset:0x7000
	s_waitcnt lgkmcnt(6)
	s_nop 0
	v_mfma_f32_32x32x16_bf16 v[112:127], v[144:147], v[128:131], v[112:127]
	ds_read_b64_tr_b16 v[192:193], v177 offset:0x200
	ds_read_b64_tr_b16 v[194:195], v177 offset:0x1200
	s_waitcnt lgkmcnt(6)
	v_mfma_f32_32x32x16_bf16 v[112:127], v[148:151], v[132:135], v[112:127]
	ds_read_b64_tr_b16 v[196:197], v177 offset:0x2200
	ds_read_b64_tr_b16 v[198:199], v177 offset:0x3200
	s_waitcnt lgkmcnt(6)
	v_mfma_f32_32x32x16_bf16 v[112:127], v[152:155], v[136:139], v[112:127]
	ds_read_b64_tr_b16 v[200:201], v177 offset:0x4200
	ds_read_b64_tr_b16 v[202:203], v177 offset:0x5200
	s_waitcnt lgkmcnt(6)
	v_mfma_f32_32x32x16_bf16 v[112:127], v[156:159], v[140:143], v[112:127]
	ds_read_b64_tr_b16 v[204:205], v177 offset:0x6200
	ds_read_b64_tr_b16 v[206:207], v177 offset:0x7200
	s_waitcnt lgkmcnt(6)
	v_mfma_f32_32x32x16_bf16 v[80:95], v[192:195], v[128:131], v[80:95]
	ds_read_b64_tr_b16 v[144:145], v177 offset:0x400
	ds_read_b64_tr_b16 v[146:147], v177 offset:0x1400
	s_waitcnt lgkmcnt(6)
	v_mfma_f32_32x32x16_bf16 v[80:95], v[196:199], v[132:135], v[80:95]
	ds_read_b64_tr_b16 v[148:149], v177 offset:0x2400
	ds_read_b64_tr_b16 v[150:151], v177 offset:0x3400
	s_waitcnt lgkmcnt(6)
	v_mfma_f32_32x32x16_bf16 v[80:95], v[200:203], v[136:139], v[80:95]
	ds_read_b64_tr_b16 v[152:153], v177 offset:0x4400
	ds_read_b64_tr_b16 v[154:155], v177 offset:0x5400
	s_waitcnt lgkmcnt(6)
	v_mfma_f32_32x32x16_bf16 v[80:95], v[204:207], v[140:143], v[80:95]
	ds_read_b64_tr_b16 v[156:157], v177 offset:0x6400
	ds_read_b64_tr_b16 v[158:159], v177 offset:0x7400
	s_waitcnt lgkmcnt(6)
	v_mfma_f32_32x32x16_bf16 v[96:111], v[144:147], v[128:131], v[96:111]
	ds_read_b64_tr_b16 v[192:193], v177 offset:0x600
	ds_read_b64_tr_b16 v[194:195], v177 offset:0x1600
	s_waitcnt lgkmcnt(6)
	v_mfma_f32_32x32x16_bf16 v[96:111], v[148:151], v[132:135], v[96:111]
	ds_read_b64_tr_b16 v[196:197], v177 offset:0x2600
	ds_read_b64_tr_b16 v[198:199], v177 offset:0x3600
	s_waitcnt lgkmcnt(6)
	v_mfma_f32_32x32x16_bf16 v[96:111], v[152:155], v[136:139], v[96:111]
	ds_read_b64_tr_b16 v[200:201], v177 offset:0x4600
	ds_read_b64_tr_b16 v[202:203], v177 offset:0x5600
	s_waitcnt lgkmcnt(6)
	v_mfma_f32_32x32x16_bf16 v[96:111], v[156:159], v[140:143], v[96:111]
	ds_read_b64_tr_b16 v[204:205], v177 offset:0x6600
	ds_read_b64_tr_b16 v[206:207], v177 offset:0x7600
	s_waitcnt lgkmcnt(6)
	v_mfma_f32_32x32x16_bf16 v[64:79], v[192:195], v[128:131], v[64:79]
	ds_read_b64_tr_b16 v[144:145], v177 offset:0x800
	ds_read_b64_tr_b16 v[146:147], v177 offset:0x1800
	s_waitcnt lgkmcnt(6)
	v_mfma_f32_32x32x16_bf16 v[64:79], v[196:199], v[132:135], v[64:79]
	ds_read_b64_tr_b16 v[148:149], v177 offset:0x2800
	ds_read_b64_tr_b16 v[150:151], v177 offset:0x3800
	s_waitcnt lgkmcnt(6)
	v_mfma_f32_32x32x16_bf16 v[64:79], v[200:203], v[136:139], v[64:79]
	ds_read_b64_tr_b16 v[152:153], v177 offset:0x4800
	ds_read_b64_tr_b16 v[154:155], v177 offset:0x5800
	s_waitcnt lgkmcnt(6)
	v_mfma_f32_32x32x16_bf16 v[64:79], v[204:207], v[140:143], v[64:79]
	ds_read_b64_tr_b16 v[156:157], v177 offset:0x6800
	ds_read_b64_tr_b16 v[158:159], v177 offset:0x7800
	s_waitcnt lgkmcnt(6)
	v_mfma_f32_32x32x16_bf16 v[48:63], v[144:147], v[128:131], v[48:63]
	ds_read_b64_tr_b16 v[192:193], v177 offset:0xa00
	ds_read_b64_tr_b16 v[194:195], v177 offset:0x1a00
	s_waitcnt lgkmcnt(6)
	v_mfma_f32_32x32x16_bf16 v[48:63], v[148:151], v[132:135], v[48:63]
	ds_read_b64_tr_b16 v[196:197], v177 offset:0x2a00
	ds_read_b64_tr_b16 v[198:199], v177 offset:0x3a00
	s_waitcnt lgkmcnt(6)
	v_mfma_f32_32x32x16_bf16 v[48:63], v[152:155], v[136:139], v[48:63]
	ds_read_b64_tr_b16 v[200:201], v177 offset:0x4a00
	ds_read_b64_tr_b16 v[202:203], v177 offset:0x5a00
	s_waitcnt lgkmcnt(6)
	v_mfma_f32_32x32x16_bf16 v[48:63], v[156:159], v[140:143], v[48:63]
	ds_read_b64_tr_b16 v[204:205], v177 offset:0x6a00
	ds_read_b64_tr_b16 v[206:207], v177 offset:0x7a00
	s_waitcnt lgkmcnt(6)
	v_mfma_f32_32x32x16_bf16 v[32:47], v[192:195], v[128:131], v[32:47]
	ds_read_b64_tr_b16 v[144:145], v177 offset:0xc00
	ds_read_b64_tr_b16 v[146:147], v177 offset:0x1c00
	s_waitcnt lgkmcnt(6)
	v_mfma_f32_32x32x16_bf16 v[32:47], v[196:199], v[132:135], v[32:47]
	ds_read_b64_tr_b16 v[148:149], v177 offset:0x2c00
	ds_read_b64_tr_b16 v[150:151], v177 offset:0x3c00
	s_waitcnt lgkmcnt(6)
	v_mfma_f32_32x32x16_bf16 v[32:47], v[200:203], v[136:139], v[32:47]
	ds_read_b64_tr_b16 v[152:153], v177 offset:0x4c00
	ds_read_b64_tr_b16 v[154:155], v177 offset:0x5c00
	s_waitcnt lgkmcnt(6)
	v_mfma_f32_32x32x16_bf16 v[32:47], v[204:207], v[140:143], v[32:47]
	ds_read_b64_tr_b16 v[156:157], v177 offset:0x6c00
	ds_read_b64_tr_b16 v[158:159], v177 offset:0x7c00
	s_waitcnt lgkmcnt(6)
	v_mfma_f32_32x32x16_bf16 v[16:31], v[144:147], v[128:131], v[16:31]
	ds_read_b64_tr_b16 v[192:193], v177 offset:0xe00
	ds_read_b64_tr_b16 v[194:195], v177 offset:0x1e00
	s_waitcnt lgkmcnt(6)
	v_mfma_f32_32x32x16_bf16 v[16:31], v[148:151], v[132:135], v[16:31]
	ds_read_b64_tr_b16 v[196:197], v177 offset:0x2e00
	ds_read_b64_tr_b16 v[198:199], v177 offset:0x3e00
	s_waitcnt lgkmcnt(6)
	v_mfma_f32_32x32x16_bf16 v[16:31], v[152:155], v[136:139], v[16:31]
	ds_read_b64_tr_b16 v[200:201], v177 offset:0x4e00
	ds_read_b64_tr_b16 v[202:203], v177 offset:0x5e00
	s_waitcnt lgkmcnt(6)
	v_mfma_f32_32x32x16_bf16 v[16:31], v[156:159], v[140:143], v[16:31]
	ds_read_b64_tr_b16 v[204:205], v177 offset:0x6e00
	ds_read_b64_tr_b16 v[206:207], v177 offset:0x7e00
	s_waitcnt lgkmcnt(6)
	v_mfma_f32_32x32x16_bf16 v[0:15], v[192:195], v[128:131], v[0:15]
	s_waitcnt lgkmcnt(4)
	v_mfma_f32_32x32x16_bf16 v[0:15], v[196:199], v[132:135], v[0:15]
	s_waitcnt lgkmcnt(2)
	v_mfma_f32_32x32x16_bf16 v[0:15], v[200:203], v[136:139], v[0:15]
	s_waitcnt lgkmcnt(0)
	v_mfma_f32_32x32x16_bf16 v[0:15], v[204:207], v[140:143], v[0:15]
	ds_read_b128 v[128:131], v188 offset:0
	ds_read_b128 v[132:135], v188 offset:0x2000
	ds_read_b128 v[192:195], v187 offset:0
	ds_read_b128 v[196:199], v187 offset:0x2000
	s_waitcnt lgkmcnt(2)
	s_nop 0
	v_mfma_f32_32x32x16_bf16 v[144:159], v[128:131], v[218:221], 0
	v_mfma_f32_32x32x16_bf16 v[128:143], v[132:135], v[218:221], 0
	ds_read_b128 v[204:207], v186 offset:0
	ds_read_b128 v[208:211], v186 offset:0x2000
	s_waitcnt lgkmcnt(2)
	v_mfma_f32_32x32x16_bf16 v[144:159], v[192:195], v[222:225], v[144:159]
	v_mfma_f32_32x32x16_bf16 v[128:143], v[196:199], v[222:225], v[128:143]
	ds_read_b128 v[192:195], v185 offset:0
	ds_read_b128 v[196:199], v185 offset:0x2000
	s_waitcnt lgkmcnt(2)
	v_mfma_f32_32x32x16_bf16 v[144:159], v[204:207], v[230:233], v[144:159]
	v_mfma_f32_32x32x16_bf16 v[128:143], v[208:211], v[230:233], v[128:143]
	ds_read_b128 v[204:207], v188 offset:0x80
	ds_read_b128 v[208:211], v188 offset:0x2080
	s_waitcnt lgkmcnt(2)
	v_mfma_f32_32x32x16_bf16 v[144:159], v[192:195], v[234:237], v[144:159]
	v_mfma_f32_32x32x16_bf16 v[128:143], v[196:199], v[234:237], v[128:143]
	ds_read_b128 v[192:195], v187 offset:0x80
	ds_read_b128 v[196:199], v187 offset:0x2080
	s_waitcnt lgkmcnt(2)
	v_mfma_f32_32x32x16_bf16 v[144:159], v[204:207], v[238:241], v[144:159]
	v_mfma_f32_32x32x16_bf16 v[128:143], v[208:211], v[238:241], v[128:143]
	ds_read_b128 v[204:207], v186 offset:0x80
	ds_read_b128 v[208:211], v186 offset:0x2080
	s_waitcnt lgkmcnt(2)
	v_mfma_f32_32x32x16_bf16 v[144:159], v[192:195], v[242:245], v[144:159]
	v_mfma_f32_32x32x16_bf16 v[128:143], v[196:199], v[242:245], v[128:143]
	ds_read_b128 v[180:183], v185 offset:0x80
	ds_read_b128 v[192:195], v185 offset:0x2080
	s_waitcnt lgkmcnt(2)
	v_mfma_f32_32x32x16_bf16 v[144:159], v[204:207], v[246:249], v[144:159]
	v_mfma_f32_32x32x16_bf16 v[128:143], v[208:211], v[246:249], v[128:143]
	s_waitcnt lgkmcnt(0)
	v_mfma_f32_32x32x16_bf16 v[144:159], v[180:183], v[166:169], v[144:159]
	v_mfma_f32_32x32x16_bf16 v[128:143], v[192:195], v[166:169], v[128:143]
	s_bitcmp0_b32 s100, 8
	s_cbranch_scc1 .Lstg_a12
	s_waitcnt vmcnt(0)
	s_waitcnt lgkmcnt(0)
	s_barrier
	s_sleep 7

.LBB0_586:
	s_or_b64 exec, exec, s[4:5]
	v_mov_b32_e32 v38, v165
	v_readlane_b32 s5, v255, 51
	v_readfirstlane_b32 s2, v38
	s_ashr_i32 s79, s2, 6
	v_bfe_u32 v0, v38, 5, 1
	v_and_b32_e32 v176, 31, v38
	s_lshl_b32 s92, s79, 5
	v_lshlrev_b32_e32 v32, 2, v0
	s_add_i32 s74, s92, s74
	v_sub_u32_e32 v1, v176, v32
	v_lshlrev_b32_e32 v175, 4, v0
	s_lshl_b32 s2, s79, 3
	v_bfe_u32 v0, v38, 4, 2
	v_add_u32_e32 v179, s74, v1
	v_or_b32_e32 v1, s2, v0
	v_and_b32_e32 v2, 15, v38
	v_and_b32_e32 v39, 63, v38
	v_bitop3_b32 v3, v0, v38, 15 bitop3:0x78
	v_mul_lo_u32 v1, v1, s14
	v_bitop3_b32 v0, v0, v2, 4 bitop3:0x36
	s_mul_i32 s4, s79, 0x1c00
	s_waitcnt vmcnt(16)
	v_lshlrev_b32_e32 v40, 4, v39
	v_lshl_or_b32 v0, v0, 4, v1
	s_lshl_b32 s78, s79, 11
	v_readlane_b32 s7, v255, 53
	s_lshl_b32 s3, s79, 12
	s_add_i32 s4, s5, s4
	v_lshl_or_b32 v160, v3, 4, v1
	v_add_u32_e32 v170, 0x1a000, v0
	s_add_i32 s78, s78, s7
	s_add_i32 s3, s3, s33
	v_add_u32_e32 v180, s4, v40
	s_waitcnt vmcnt(16) lgkmcnt(0)
	v_mov_b64_e32 v[218:219], v[128:129]
	v_mov_b64_e32 v[220:221], v[130:131]
	v_mov_b64_e32 v[222:223], v[132:133]
	v_mov_b64_e32 v[224:225], v[134:135]
	v_mov_b64_e32 v[230:231], v[136:137]
	v_mov_b64_e32 v[232:233], v[138:139]
	v_mov_b64_e32 v[234:235], v[140:141]
	v_mov_b64_e32 v[236:237], v[142:143]
	v_mov_b64_e32 v[238:239], v[144:145]
	v_mov_b64_e32 v[240:241], v[146:147]
	v_mov_b64_e32 v[242:243], v[148:149]
	v_mov_b64_e32 v[244:245], v[150:151]
	v_mov_b64_e32 v[246:247], v[152:153]
	v_mov_b64_e32 v[248:249], v[154:155]
	s_add_u32 s4, s66, 0x1a2900
	s_addc_u32 s5, s67, 0
	v_lshl_add_u64 v[0:1], s[4:5], 0, v[160:161]
	s_add_i32 s82, s78, 0x4000
	s_mov_b32 s6, m0
	s_mov_b32 m0, s82
	s_nop 0
	global_load_lds_dwordx4 v[0:1], off
	s_mov_b32 m0, s6
	v_mov_b32_e32 v171, v161
	v_lshl_add_u64 v[0:1], s[4:5], 0, v[170:171]
	s_add_i32 s84, s78, 0x4400
	s_mov_b32 s4, m0
	s_mov_b32 m0, s84
	s_nop 0
	global_load_lds_dwordx4 v[0:1], off
	s_mov_b32 m0, s4
	s_waitcnt lgkmcnt(0)
	s_barrier
	v_lshlrev_b32_e32 v0, 4, v38
	s_movk_i32 s4, 0x70
	v_lshlrev_b32_e32 v33, 8, v176
	v_and_b32_e32 v1, 0x70, v0
	v_bitop3_b32 v34, v175, v0, s4 bitop3:0x78
	s_movk_i32 s4, 0x60
	v_add_u32_e32 v2, s7, v33
	v_bitop3_b32 v35, v175, v1, 32 bitop3:0x36
	v_bitop3_b32 v36, v175, v1, 64 bitop3:0x36
	v_bitop3_b32 v37, v175, v1, s4 bitop3:0x36
	v_add_u32_e32 v181, v34, v2
	v_add_u32_e32 v182, v35, v2
	v_add_u32_e32 v183, v36, v2
	v_add_u32_e32 v184, v37, v2
	ds_read_b128 v[0:3], v181 offset:0
	ds_read_b128 v[4:7], v181 offset:0x2000
	ds_read_b128 v[42:45], v182 offset:0
	ds_read_b128 v[46:49], v182 offset:0x2000
	s_waitcnt lgkmcnt(2)
	s_nop 0
	v_mfma_f32_32x32x16_bf16 v[16:31], v[0:3], v[218:221], 0
	v_mfma_f32_32x32x16_bf16 v[0:15], v[4:7], v[218:221], 0
	ds_read_b128 v[54:57], v183 offset:0
	ds_read_b128 v[58:61], v183 offset:0x2000
	s_waitcnt lgkmcnt(2)
	v_mfma_f32_32x32x16_bf16 v[16:31], v[42:45], v[222:225], v[16:31]
	v_mfma_f32_32x32x16_bf16 v[0:15], v[46:49], v[222:225], v[0:15]
	ds_read_b128 v[42:45], v184 offset:0
	ds_read_b128 v[46:49], v184 offset:0x2000
	s_waitcnt lgkmcnt(2)
	v_mfma_f32_32x32x16_bf16 v[16:31], v[54:57], v[230:233], v[16:31]
	v_mfma_f32_32x32x16_bf16 v[0:15], v[58:61], v[230:233], v[0:15]
	ds_read_b128 v[54:57], v181 offset:0x80
	ds_read_b128 v[58:61], v181 offset:0x2080
	s_waitcnt lgkmcnt(2)
	v_mfma_f32_32x32x16_bf16 v[16:31], v[42:45], v[234:237], v[16:31]
	v_mfma_f32_32x32x16_bf16 v[0:15], v[46:49], v[234:237], v[0:15]
	ds_read_b128 v[42:45], v182 offset:0x80
	ds_read_b128 v[46:49], v182 offset:0x2080
	s_waitcnt lgkmcnt(2)
	v_mfma_f32_32x32x16_bf16 v[16:31], v[54:57], v[238:241], v[16:31]
	v_mfma_f32_32x32x16_bf16 v[0:15], v[58:61], v[238:241], v[0:15]
	ds_read_b128 v[54:57], v183 offset:0x80
	ds_read_b128 v[58:61], v183 offset:0x2080
	s_waitcnt lgkmcnt(2)
	v_mfma_f32_32x32x16_bf16 v[16:31], v[42:45], v[242:245], v[16:31]
	v_mfma_f32_32x32x16_bf16 v[0:15], v[46:49], v[242:245], v[0:15]
	ds_read_b128 v[42:45], v184 offset:0x80
	ds_read_b128 v[46:49], v184 offset:0x2080
	s_waitcnt lgkmcnt(2)
	v_mfma_f32_32x32x16_bf16 v[16:31], v[54:57], v[246:249], v[16:31]
	v_mfma_f32_32x32x16_bf16 v[0:15], v[58:61], v[246:249], v[0:15]
	s_waitcnt lgkmcnt(0)
	v_mfma_f32_32x32x16_bf16 v[16:31], v[42:45], v[166:169], v[16:31]
	v_mfma_f32_32x32x16_bf16 v[0:15], v[46:49], v[166:169], v[0:15]
	s_bitcmp0_b32 s100, 8
	s_cbranch_scc1 .Lstg_a17
	s_waitcnt vmcnt(0)
	s_waitcnt lgkmcnt(0)
	s_barrier
	s_sleep 7

.LBB0_589:
	ds_read_b64_tr_b16 v[144:145], v177 offset:0
	ds_read_b64_tr_b16 v[146:147], v177 offset:0x1000
	ds_read_b64_tr_b16 v[148:149], v177 offset:0x2000
	ds_read_b64_tr_b16 v[150:151], v177 offset:0x3000
	ds_read_b64_tr_b16 v[152:153], v177 offset:0x4000
	ds_read_b64_tr_b16 v[154:155], v177 offset:0x5000
	ds_read_b64_tr_b16 v[156:157], v177 offset:0x6000
	ds_read_b64_tr_b16 v[158:159], v177 offset:0x7000
	s_waitcnt lgkmcnt(6)
	s_nop 0
	v_mfma_f32_32x32x16_bf16 v[112:127], v[144:147], v[128:131], v[112:127]
	ds_read_b64_tr_b16 v[192:193], v177 offset:0x200
	ds_read_b64_tr_b16 v[194:195], v177 offset:0x1200
	s_waitcnt lgkmcnt(6)
	v_mfma_f32_32x32x16_bf16 v[112:127], v[148:151], v[132:135], v[112:127]
	ds_read_b64_tr_b16 v[196:197], v177 offset:0x2200
	ds_read_b64_tr_b16 v[198:199], v177 offset:0x3200
	s_waitcnt lgkmcnt(6)
	v_mfma_f32_32x32x16_bf16 v[112:127], v[152:155], v[136:139], v[112:127]
	ds_read_b64_tr_b16 v[200:201], v177 offset:0x4200
	ds_read_b64_tr_b16 v[202:203], v177 offset:0x5200
	s_waitcnt lgkmcnt(6)
	v_mfma_f32_32x32x16_bf16 v[112:127], v[156:159], v[140:143], v[112:127]
	ds_read_b64_tr_b16 v[204:205], v177 offset:0x6200
	ds_read_b64_tr_b16 v[206:207], v177 offset:0x7200
	s_waitcnt lgkmcnt(6)
	v_mfma_f32_32x32x16_bf16 v[96:111], v[192:195], v[128:131], v[96:111]
	ds_read_b64_tr_b16 v[144:145], v177 offset:0x400
	ds_read_b64_tr_b16 v[146:147], v177 offset:0x1400
	s_waitcnt lgkmcnt(6)
	v_mfma_f32_32x32x16_bf16 v[96:111], v[196:199], v[132:135], v[96:111]
	ds_read_b64_tr_b16 v[148:149], v177 offset:0x2400
	ds_read_b64_tr_b16 v[150:151], v177 offset:0x3400
	s_waitcnt lgkmcnt(6)
	v_mfma_f32_32x32x16_bf16 v[96:111], v[200:203], v[136:139], v[96:111]
	ds_read_b64_tr_b16 v[152:153], v177 offset:0x4400
	ds_read_b64_tr_b16 v[154:155], v177 offset:0x5400
	s_waitcnt lgkmcnt(6)
	v_mfma_f32_32x32x16_bf16 v[96:111], v[204:207], v[140:143], v[96:111]
	ds_read_b64_tr_b16 v[156:157], v177 offset:0x6400
	ds_read_b64_tr_b16 v[158:159], v177 offset:0x7400
	s_waitcnt lgkmcnt(6)
	v_mfma_f32_32x32x16_bf16 v[80:95], v[144:147], v[128:131], v[80:95]
	ds_read_b64_tr_b16 v[192:193], v177 offset:0x600
	ds_read_b64_tr_b16 v[194:195], v177 offset:0x1600
	s_waitcnt lgkmcnt(6)
	v_mfma_f32_32x32x16_bf16 v[80:95], v[148:151], v[132:135], v[80:95]
	ds_read_b64_tr_b16 v[196:197], v177 offset:0x2600
	ds_read_b64_tr_b16 v[198:199], v177 offset:0x3600
	s_waitcnt lgkmcnt(6)
	v_mfma_f32_32x32x16_bf16 v[80:95], v[152:155], v[136:139], v[80:95]
	ds_read_b64_tr_b16 v[200:201], v177 offset:0x4600
	ds_read_b64_tr_b16 v[202:203], v177 offset:0x5600
	s_waitcnt lgkmcnt(6)
	v_mfma_f32_32x32x16_bf16 v[80:95], v[156:159], v[140:143], v[80:95]
	ds_read_b64_tr_b16 v[204:205], v177 offset:0x6600
	ds_read_b64_tr_b16 v[206:207], v177 offset:0x7600
	s_waitcnt lgkmcnt(6)
	v_mfma_f32_32x32x16_bf16 v[64:79], v[192:195], v[128:131], v[64:79]
	ds_read_b64_tr_b16 v[144:145], v177 offset:0x800
	ds_read_b64_tr_b16 v[146:147], v177 offset:0x1800
	s_waitcnt lgkmcnt(6)
	v_mfma_f32_32x32x16_bf16 v[64:79], v[196:199], v[132:135], v[64:79]
	ds_read_b64_tr_b16 v[148:149], v177 offset:0x2800
	ds_read_b64_tr_b16 v[150:151], v177 offset:0x3800
	s_waitcnt lgkmcnt(6)
	v_mfma_f32_32x32x16_bf16 v[64:79], v[200:203], v[136:139], v[64:79]
	ds_read_b64_tr_b16 v[152:153], v177 offset:0x4800
	ds_read_b64_tr_b16 v[154:155], v177 offset:0x5800
	s_waitcnt lgkmcnt(6)
	v_mfma_f32_32x32x16_bf16 v[64:79], v[204:207], v[140:143], v[64:79]
	ds_read_b64_tr_b16 v[156:157], v177 offset:0x6800
	ds_read_b64_tr_b16 v[158:159], v177 offset:0x7800
	s_waitcnt lgkmcnt(6)
	v_mfma_f32_32x32x16_bf16 v[48:63], v[144:147], v[128:131], v[48:63]
	ds_read_b64_tr_b16 v[192:193], v177 offset:0xa00
	ds_read_b64_tr_b16 v[194:195], v177 offset:0x1a00
	s_waitcnt lgkmcnt(6)
	v_mfma_f32_32x32x16_bf16 v[48:63], v[148:151], v[132:135], v[48:63]
	ds_read_b64_tr_b16 v[196:197], v177 offset:0x2a00
	ds_read_b64_tr_b16 v[198:199], v177 offset:0x3a00
	s_waitcnt lgkmcnt(6)
	v_mfma_f32_32x32x16_bf16 v[48:63], v[152:155], v[136:139], v[48:63]
	ds_read_b64_tr_b16 v[200:201], v177 offset:0x4a00
	ds_read_b64_tr_b16 v[202:203], v177 offset:0x5a00
	s_waitcnt lgkmcnt(6)
	v_mfma_f32_32x32x16_bf16 v[48:63], v[156:159], v[140:143], v[48:63]
	ds_read_b64_tr_b16 v[204:205], v177 offset:0x6a00
	ds_read_b64_tr_b16 v[206:207], v177 offset:0x7a00
	s_waitcnt lgkmcnt(6)
	v_mfma_f32_32x32x16_bf16 v[32:47], v[192:195], v[128:131], v[32:47]
	ds_read_b64_tr_b16 v[144:145], v177 offset:0xc00
	ds_read_b64_tr_b16 v[146:147], v177 offset:0x1c00
	s_waitcnt lgkmcnt(6)
	v_mfma_f32_32x32x16_bf16 v[32:47], v[196:199], v[132:135], v[32:47]
	ds_read_b64_tr_b16 v[148:149], v177 offset:0x2c00
	ds_read_b64_tr_b16 v[150:151], v177 offset:0x3c00
	s_waitcnt lgkmcnt(6)
	v_mfma_f32_32x32x16_bf16 v[32:47], v[200:203], v[136:139], v[32:47]
	ds_read_b64_tr_b16 v[152:153], v177 offset:0x4c00
	ds_read_b64_tr_b16 v[154:155], v177 offset:0x5c00
	s_waitcnt lgkmcnt(6)
	v_mfma_f32_32x32x16_bf16 v[32:47], v[204:207], v[140:143], v[32:47]
	ds_read_b64_tr_b16 v[156:157], v177 offset:0x6c00
	ds_read_b64_tr_b16 v[158:159], v177 offset:0x7c00
	s_waitcnt lgkmcnt(6)
	v_mfma_f32_32x32x16_bf16 v[16:31], v[144:147], v[128:131], v[16:31]
	ds_read_b64_tr_b16 v[192:193], v177 offset:0xe00
	ds_read_b64_tr_b16 v[194:195], v177 offset:0x1e00
	s_waitcnt lgkmcnt(6)
	v_mfma_f32_32x32x16_bf16 v[16:31], v[148:151], v[132:135], v[16:31]
	ds_read_b64_tr_b16 v[196:197], v177 offset:0x2e00
	ds_read_b64_tr_b16 v[198:199], v177 offset:0x3e00
	s_waitcnt lgkmcnt(6)
	v_mfma_f32_32x32x16_bf16 v[16:31], v[152:155], v[136:139], v[16:31]
	ds_read_b64_tr_b16 v[200:201], v177 offset:0x4e00
	ds_read_b64_tr_b16 v[202:203], v177 offset:0x5e00
	s_waitcnt lgkmcnt(6)
	v_mfma_f32_32x32x16_bf16 v[16:31], v[156:159], v[140:143], v[16:31]
	ds_read_b64_tr_b16 v[204:205], v177 offset:0x6e00
	ds_read_b64_tr_b16 v[206:207], v177 offset:0x7e00
	s_waitcnt lgkmcnt(6)
	v_mfma_f32_32x32x16_bf16 v[0:15], v[192:195], v[128:131], v[0:15]
	s_waitcnt lgkmcnt(4)
	v_mfma_f32_32x32x16_bf16 v[0:15], v[196:199], v[132:135], v[0:15]
	s_waitcnt lgkmcnt(2)
	v_mfma_f32_32x32x16_bf16 v[0:15], v[200:203], v[136:139], v[0:15]
	s_waitcnt lgkmcnt(0)
	v_mfma_f32_32x32x16_bf16 v[0:15], v[204:207], v[140:143], v[0:15]
	ds_read_b128 v[128:131], v188 offset:0
	ds_read_b128 v[132:135], v188 offset:0x2000
	ds_read_b128 v[192:195], v187 offset:0
	ds_read_b128 v[196:199], v187 offset:0x2000
	s_waitcnt lgkmcnt(2)
	s_nop 0
	v_mfma_f32_32x32x16_bf16 v[144:159], v[128:131], v[218:221], 0
	v_mfma_f32_32x32x16_bf16 v[128:143], v[132:135], v[218:221], 0
	ds_read_b128 v[204:207], v186 offset:0
	ds_read_b128 v[208:211], v186 offset:0x2000
	s_waitcnt lgkmcnt(2)
	v_mfma_f32_32x32x16_bf16 v[144:159], v[192:195], v[222:225], v[144:159]
	v_mfma_f32_32x32x16_bf16 v[128:143], v[196:199], v[222:225], v[128:143]
	ds_read_b128 v[192:195], v185 offset:0
	ds_read_b128 v[196:199], v185 offset:0x2000
	s_waitcnt lgkmcnt(2)
	v_mfma_f32_32x32x16_bf16 v[144:159], v[204:207], v[230:233], v[144:159]
	v_mfma_f32_32x32x16_bf16 v[128:143], v[208:211], v[230:233], v[128:143]
	ds_read_b128 v[204:207], v188 offset:0x80
	ds_read_b128 v[208:211], v188 offset:0x2080
	s_waitcnt lgkmcnt(2)
	v_mfma_f32_32x32x16_bf16 v[144:159], v[192:195], v[234:237], v[144:159]
	v_mfma_f32_32x32x16_bf16 v[128:143], v[196:199], v[234:237], v[128:143]
	ds_read_b128 v[192:195], v187 offset:0x80
	ds_read_b128 v[196:199], v187 offset:0x2080
	s_waitcnt lgkmcnt(2)
	v_mfma_f32_32x32x16_bf16 v[144:159], v[204:207], v[238:241], v[144:159]
	v_mfma_f32_32x32x16_bf16 v[128:143], v[208:211], v[238:241], v[128:143]
	ds_read_b128 v[204:207], v186 offset:0x80
	ds_read_b128 v[208:211], v186 offset:0x2080
	s_waitcnt lgkmcnt(2)
	v_mfma_f32_32x32x16_bf16 v[144:159], v[192:195], v[242:245], v[144:159]
	v_mfma_f32_32x32x16_bf16 v[128:143], v[196:199], v[242:245], v[128:143]
	ds_read_b128 v[192:195], v185 offset:0x80
	ds_read_b128 v[196:199], v185 offset:0x2080
	s_waitcnt lgkmcnt(2)
	v_mfma_f32_32x32x16_bf16 v[144:159], v[204:207], v[246:249], v[144:159]
	v_mfma_f32_32x32x16_bf16 v[128:143], v[208:211], v[246:249], v[128:143]
	s_waitcnt lgkmcnt(0)
	v_mfma_f32_32x32x16_bf16 v[144:159], v[192:195], v[166:169], v[144:159]
	v_mfma_f32_32x32x16_bf16 v[128:143], v[196:199], v[166:169], v[128:143]
	s_bitcmp0_b32 s100, 8
	s_cbranch_scc1 .Lstg_a18
	s_waitcnt vmcnt(0)
	s_waitcnt lgkmcnt(0)
	s_barrier
	s_sleep 7

.LBB0_597:
	ds_read_b64_tr_b16 v[144:145], v177 offset:0x8000
	ds_read_b64_tr_b16 v[146:147], v177 offset:0x9000
	ds_read_b64_tr_b16 v[148:149], v177 offset:0xa000
	ds_read_b64_tr_b16 v[150:151], v177 offset:0xb000
	ds_read_b64_tr_b16 v[152:153], v177 offset:0xc000
	ds_read_b64_tr_b16 v[154:155], v177 offset:0xd000
	ds_read_b64_tr_b16 v[156:157], v177 offset:0xe000
	ds_read_b64_tr_b16 v[158:159], v177 offset:0xf000
	s_waitcnt lgkmcnt(6)
	s_nop 0
	v_mfma_f32_32x32x16_bf16 v[112:127], v[144:147], v[128:131], v[112:127]
	ds_read_b64_tr_b16 v[194:195], v177 offset:0x8200
	ds_read_b64_tr_b16 v[196:197], v177 offset:0x9200
	s_waitcnt lgkmcnt(6)
	v_mfma_f32_32x32x16_bf16 v[112:127], v[148:151], v[132:135], v[112:127]
	ds_read_b64_tr_b16 v[198:199], v177 offset:0xa200
	ds_read_b64_tr_b16 v[200:201], v177 offset:0xb200
	s_waitcnt lgkmcnt(6)
	v_mfma_f32_32x32x16_bf16 v[112:127], v[152:155], v[136:139], v[112:127]
	ds_read_b64_tr_b16 v[202:203], v177 offset:0xc200
	ds_read_b64_tr_b16 v[204:205], v177 offset:0xd200
	s_waitcnt lgkmcnt(6)
	v_mfma_f32_32x32x16_bf16 v[112:127], v[156:159], v[140:143], v[112:127]
	ds_read_b64_tr_b16 v[206:207], v177 offset:0xe200
	ds_read_b64_tr_b16 v[208:209], v177 offset:0xf200
	s_waitcnt lgkmcnt(6)
	v_mfma_f32_32x32x16_bf16 v[96:111], v[194:197], v[128:131], v[96:111]
	ds_read_b64_tr_b16 v[144:145], v177 offset:0x8400
	ds_read_b64_tr_b16 v[146:147], v177 offset:0x9400
	s_waitcnt lgkmcnt(6)
	v_mfma_f32_32x32x16_bf16 v[96:111], v[198:201], v[132:135], v[96:111]
	ds_read_b64_tr_b16 v[148:149], v177 offset:0xa400
	ds_read_b64_tr_b16 v[150:151], v177 offset:0xb400
	s_waitcnt lgkmcnt(6)
	v_mfma_f32_32x32x16_bf16 v[96:111], v[202:205], v[136:139], v[96:111]
	ds_read_b64_tr_b16 v[152:153], v177 offset:0xc400
	ds_read_b64_tr_b16 v[154:155], v177 offset:0xd400
	s_waitcnt lgkmcnt(6)
	v_mfma_f32_32x32x16_bf16 v[96:111], v[206:209], v[140:143], v[96:111]
	ds_read_b64_tr_b16 v[156:157], v177 offset:0xe400
	ds_read_b64_tr_b16 v[158:159], v177 offset:0xf400
	s_waitcnt lgkmcnt(6)
	v_mfma_f32_32x32x16_bf16 v[80:95], v[144:147], v[128:131], v[80:95]
	ds_read_b64_tr_b16 v[194:195], v177 offset:0x8600
	ds_read_b64_tr_b16 v[196:197], v177 offset:0x9600
	s_waitcnt lgkmcnt(6)
	v_mfma_f32_32x32x16_bf16 v[80:95], v[148:151], v[132:135], v[80:95]
	ds_read_b64_tr_b16 v[198:199], v177 offset:0xa600
	ds_read_b64_tr_b16 v[200:201], v177 offset:0xb600
	s_waitcnt lgkmcnt(6)
	v_mfma_f32_32x32x16_bf16 v[80:95], v[152:155], v[136:139], v[80:95]
	ds_read_b64_tr_b16 v[202:203], v177 offset:0xc600
	ds_read_b64_tr_b16 v[204:205], v177 offset:0xd600
	s_waitcnt lgkmcnt(6)
	v_mfma_f32_32x32x16_bf16 v[80:95], v[156:159], v[140:143], v[80:95]
	ds_read_b64_tr_b16 v[206:207], v177 offset:0xe600
	ds_read_b64_tr_b16 v[208:209], v177 offset:0xf600
	s_waitcnt lgkmcnt(6)
	v_mfma_f32_32x32x16_bf16 v[64:79], v[194:197], v[128:131], v[64:79]
	ds_read_b64_tr_b16 v[144:145], v177 offset:0x8800
	ds_read_b64_tr_b16 v[146:147], v177 offset:0x9800
	s_waitcnt lgkmcnt(6)
	v_mfma_f32_32x32x16_bf16 v[64:79], v[198:201], v[132:135], v[64:79]
	ds_read_b64_tr_b16 v[148:149], v177 offset:0xa800
	ds_read_b64_tr_b16 v[150:151], v177 offset:0xb800
	s_waitcnt lgkmcnt(6)
	v_mfma_f32_32x32x16_bf16 v[64:79], v[202:205], v[136:139], v[64:79]
	ds_read_b64_tr_b16 v[152:153], v177 offset:0xc800
	ds_read_b64_tr_b16 v[154:155], v177 offset:0xd800
	s_waitcnt lgkmcnt(6)
	v_mfma_f32_32x32x16_bf16 v[64:79], v[206:209], v[140:143], v[64:79]
	ds_read_b64_tr_b16 v[156:157], v177 offset:0xe800
	ds_read_b64_tr_b16 v[158:159], v177 offset:0xf800
	s_waitcnt lgkmcnt(6)
	v_mfma_f32_32x32x16_bf16 v[48:63], v[144:147], v[128:131], v[48:63]
	ds_read_b64_tr_b16 v[194:195], v177 offset:0x8a00
	ds_read_b64_tr_b16 v[196:197], v177 offset:0x9a00
	s_waitcnt lgkmcnt(6)
	v_mfma_f32_32x32x16_bf16 v[48:63], v[148:151], v[132:135], v[48:63]
	ds_read_b64_tr_b16 v[198:199], v177 offset:0xaa00
	ds_read_b64_tr_b16 v[200:201], v177 offset:0xba00
	s_waitcnt lgkmcnt(6)
	v_mfma_f32_32x32x16_bf16 v[48:63], v[152:155], v[136:139], v[48:63]
	ds_read_b64_tr_b16 v[202:203], v177 offset:0xca00
	ds_read_b64_tr_b16 v[204:205], v177 offset:0xda00
	s_waitcnt lgkmcnt(6)
	v_mfma_f32_32x32x16_bf16 v[48:63], v[156:159], v[140:143], v[48:63]
	ds_read_b64_tr_b16 v[206:207], v177 offset:0xea00
	ds_read_b64_tr_b16 v[208:209], v177 offset:0xfa00
	s_waitcnt lgkmcnt(6)
	v_mfma_f32_32x32x16_bf16 v[32:47], v[194:197], v[128:131], v[32:47]
	ds_read_b64_tr_b16 v[144:145], v177 offset:0x8c00
	ds_read_b64_tr_b16 v[146:147], v177 offset:0x9c00
	s_waitcnt lgkmcnt(6)
	v_mfma_f32_32x32x16_bf16 v[32:47], v[198:201], v[132:135], v[32:47]
	ds_read_b64_tr_b16 v[148:149], v177 offset:0xac00
	ds_read_b64_tr_b16 v[150:151], v177 offset:0xbc00
	s_waitcnt lgkmcnt(6)
	v_mfma_f32_32x32x16_bf16 v[32:47], v[202:205], v[136:139], v[32:47]
	ds_read_b64_tr_b16 v[152:153], v177 offset:0xcc00
	ds_read_b64_tr_b16 v[154:155], v177 offset:0xdc00
	s_waitcnt lgkmcnt(6)
	v_mfma_f32_32x32x16_bf16 v[32:47], v[206:209], v[140:143], v[32:47]
	ds_read_b64_tr_b16 v[156:157], v177 offset:0xec00
	ds_read_b64_tr_b16 v[158:159], v177 offset:0xfc00
	s_waitcnt lgkmcnt(6)
	v_mfma_f32_32x32x16_bf16 v[16:31], v[144:147], v[128:131], v[16:31]
	ds_read_b64_tr_b16 v[194:195], v177 offset:0x8e00
	ds_read_b64_tr_b16 v[196:197], v177 offset:0x9e00
	s_waitcnt lgkmcnt(6)
	v_mfma_f32_32x32x16_bf16 v[16:31], v[148:151], v[132:135], v[16:31]
	ds_read_b64_tr_b16 v[198:199], v177 offset:0xae00
	ds_read_b64_tr_b16 v[200:201], v177 offset:0xbe00
	s_waitcnt lgkmcnt(6)
	v_mfma_f32_32x32x16_bf16 v[16:31], v[152:155], v[136:139], v[16:31]
	ds_read_b64_tr_b16 v[202:203], v177 offset:0xce00
	ds_read_b64_tr_b16 v[204:205], v177 offset:0xde00
	s_waitcnt lgkmcnt(6)
	v_mfma_f32_32x32x16_bf16 v[16:31], v[156:159], v[140:143], v[16:31]
	ds_read_b64_tr_b16 v[206:207], v177 offset:0xee00
	ds_read_b64_tr_b16 v[208:209], v177 offset:0xfe00
	s_waitcnt lgkmcnt(6)
	v_mfma_f32_32x32x16_bf16 v[0:15], v[194:197], v[128:131], v[0:15]
	s_waitcnt lgkmcnt(4)
	v_mfma_f32_32x32x16_bf16 v[0:15], v[198:201], v[132:135], v[0:15]
	s_waitcnt lgkmcnt(2)
	v_mfma_f32_32x32x16_bf16 v[0:15], v[202:205], v[136:139], v[0:15]
	s_waitcnt lgkmcnt(0)
	v_mfma_f32_32x32x16_bf16 v[0:15], v[206:209], v[140:143], v[0:15]
	ds_read_b128 v[128:131], v181 offset:0
	ds_read_b128 v[132:135], v181 offset:0x2000
	ds_read_b128 v[194:197], v182 offset:0
	ds_read_b128 v[198:201], v182 offset:0x2000
	s_waitcnt lgkmcnt(2)
	s_nop 0
	v_mfma_f32_32x32x16_bf16 v[144:159], v[128:131], v[218:221], 0
	v_mfma_f32_32x32x16_bf16 v[128:143], v[132:135], v[218:221], 0
	ds_read_b128 v[206:209], v183 offset:0
	ds_read_b128 v[210:213], v183 offset:0x2000
	s_waitcnt lgkmcnt(2)
	v_mfma_f32_32x32x16_bf16 v[144:159], v[194:197], v[222:225], v[144:159]
	v_mfma_f32_32x32x16_bf16 v[128:143], v[198:201], v[222:225], v[128:143]
	ds_read_b128 v[194:197], v184 offset:0
	ds_read_b128 v[198:201], v184 offset:0x2000
	s_waitcnt lgkmcnt(2)
	v_mfma_f32_32x32x16_bf16 v[144:159], v[206:209], v[230:233], v[144:159]
	v_mfma_f32_32x32x16_bf16 v[128:143], v[210:213], v[230:233], v[128:143]
	ds_read_b128 v[206:209], v181 offset:0x80
	ds_read_b128 v[210:213], v181 offset:0x2080
	s_waitcnt lgkmcnt(2)
	v_mfma_f32_32x32x16_bf16 v[144:159], v[194:197], v[234:237], v[144:159]
	v_mfma_f32_32x32x16_bf16 v[128:143], v[198:201], v[234:237], v[128:143]
	ds_read_b128 v[194:197], v182 offset:0x80
	ds_read_b128 v[198:201], v182 offset:0x2080
	s_waitcnt lgkmcnt(2)
	v_mfma_f32_32x32x16_bf16 v[144:159], v[206:209], v[238:241], v[144:159]
	v_mfma_f32_32x32x16_bf16 v[128:143], v[210:213], v[238:241], v[128:143]
	ds_read_b128 v[206:209], v183 offset:0x80
	ds_read_b128 v[210:213], v183 offset:0x2080
	s_waitcnt lgkmcnt(2)
	v_mfma_f32_32x32x16_bf16 v[144:159], v[194:197], v[242:245], v[144:159]
	v_mfma_f32_32x32x16_bf16 v[128:143], v[198:201], v[242:245], v[128:143]
	ds_read_b128 v[194:197], v184 offset:0x80
	ds_read_b128 v[198:201], v184 offset:0x2080
	s_waitcnt lgkmcnt(2)
	v_mfma_f32_32x32x16_bf16 v[144:159], v[206:209], v[246:249], v[144:159]
	v_mfma_f32_32x32x16_bf16 v[128:143], v[210:213], v[246:249], v[128:143]
	s_waitcnt lgkmcnt(0)
	v_mfma_f32_32x32x16_bf16 v[144:159], v[194:197], v[166:169], v[144:159]
	v_mfma_f32_32x32x16_bf16 v[128:143], v[198:201], v[166:169], v[128:143]
	s_bitcmp0_b32 s100, 8
	s_cbranch_scc1 .Lstg_a19
	s_waitcnt vmcnt(0)
	s_waitcnt lgkmcnt(0)
	s_barrier
	s_sleep 7

.LBB0_612:
	ds_read_b64_tr_b16 v[144:145], v177 offset:0
	ds_read_b64_tr_b16 v[146:147], v177 offset:0x1000
	ds_read_b64_tr_b16 v[148:149], v177 offset:0x2000
	ds_read_b64_tr_b16 v[150:151], v177 offset:0x3000
	ds_read_b64_tr_b16 v[152:153], v177 offset:0x4000
	ds_read_b64_tr_b16 v[154:155], v177 offset:0x5000
	ds_read_b64_tr_b16 v[156:157], v177 offset:0x6000
	ds_read_b64_tr_b16 v[158:159], v177 offset:0x7000
	s_waitcnt lgkmcnt(6)
	s_nop 0
	v_mfma_f32_32x32x16_bf16 v[112:127], v[144:147], v[128:131], v[112:127]
	ds_read_b64_tr_b16 v[192:193], v177 offset:0x200
	ds_read_b64_tr_b16 v[194:195], v177 offset:0x1200
	s_waitcnt lgkmcnt(6)
	v_mfma_f32_32x32x16_bf16 v[112:127], v[148:151], v[132:135], v[112:127]
	ds_read_b64_tr_b16 v[196:197], v177 offset:0x2200
	ds_read_b64_tr_b16 v[198:199], v177 offset:0x3200
	s_waitcnt lgkmcnt(6)
	v_mfma_f32_32x32x16_bf16 v[112:127], v[152:155], v[136:139], v[112:127]
	ds_read_b64_tr_b16 v[200:201], v177 offset:0x4200
	ds_read_b64_tr_b16 v[202:203], v177 offset:0x5200
	s_waitcnt lgkmcnt(6)
	v_mfma_f32_32x32x16_bf16 v[112:127], v[156:159], v[140:143], v[112:127]
	ds_read_b64_tr_b16 v[204:205], v177 offset:0x6200
	ds_read_b64_tr_b16 v[206:207], v177 offset:0x7200
	s_waitcnt lgkmcnt(6)
	v_mfma_f32_32x32x16_bf16 v[96:111], v[192:195], v[128:131], v[96:111]
	ds_read_b64_tr_b16 v[144:145], v177 offset:0x400
	ds_read_b64_tr_b16 v[146:147], v177 offset:0x1400
	s_waitcnt lgkmcnt(6)
	v_mfma_f32_32x32x16_bf16 v[96:111], v[196:199], v[132:135], v[96:111]
	ds_read_b64_tr_b16 v[148:149], v177 offset:0x2400
	ds_read_b64_tr_b16 v[150:151], v177 offset:0x3400
	s_waitcnt lgkmcnt(6)
	v_mfma_f32_32x32x16_bf16 v[96:111], v[200:203], v[136:139], v[96:111]
	ds_read_b64_tr_b16 v[152:153], v177 offset:0x4400
	ds_read_b64_tr_b16 v[154:155], v177 offset:0x5400
	s_waitcnt lgkmcnt(6)
	v_mfma_f32_32x32x16_bf16 v[96:111], v[204:207], v[140:143], v[96:111]
	ds_read_b64_tr_b16 v[156:157], v177 offset:0x6400
	ds_read_b64_tr_b16 v[158:159], v177 offset:0x7400
	s_waitcnt lgkmcnt(6)
	v_mfma_f32_32x32x16_bf16 v[80:95], v[144:147], v[128:131], v[80:95]
	ds_read_b64_tr_b16 v[192:193], v177 offset:0x600
	ds_read_b64_tr_b16 v[194:195], v177 offset:0x1600
	s_waitcnt lgkmcnt(6)
	v_mfma_f32_32x32x16_bf16 v[80:95], v[148:151], v[132:135], v[80:95]
	ds_read_b64_tr_b16 v[196:197], v177 offset:0x2600
	ds_read_b64_tr_b16 v[198:199], v177 offset:0x3600
	s_waitcnt lgkmcnt(6)
	v_mfma_f32_32x32x16_bf16 v[80:95], v[152:155], v[136:139], v[80:95]
	ds_read_b64_tr_b16 v[200:201], v177 offset:0x4600
	ds_read_b64_tr_b16 v[202:203], v177 offset:0x5600
	s_waitcnt lgkmcnt(6)
	v_mfma_f32_32x32x16_bf16 v[80:95], v[156:159], v[140:143], v[80:95]
	ds_read_b64_tr_b16 v[204:205], v177 offset:0x6600
	ds_read_b64_tr_b16 v[206:207], v177 offset:0x7600
	s_waitcnt lgkmcnt(6)
	v_mfma_f32_32x32x16_bf16 v[64:79], v[192:195], v[128:131], v[64:79]
	ds_read_b64_tr_b16 v[144:145], v177 offset:0x800
	ds_read_b64_tr_b16 v[146:147], v177 offset:0x1800
	s_waitcnt lgkmcnt(6)
	v_mfma_f32_32x32x16_bf16 v[64:79], v[196:199], v[132:135], v[64:79]
	ds_read_b64_tr_b16 v[148:149], v177 offset:0x2800
	ds_read_b64_tr_b16 v[150:151], v177 offset:0x3800
	s_waitcnt lgkmcnt(6)
	v_mfma_f32_32x32x16_bf16 v[64:79], v[200:203], v[136:139], v[64:79]
	ds_read_b64_tr_b16 v[152:153], v177 offset:0x4800
	ds_read_b64_tr_b16 v[154:155], v177 offset:0x5800
	s_waitcnt lgkmcnt(6)
	v_mfma_f32_32x32x16_bf16 v[64:79], v[204:207], v[140:143], v[64:79]
	ds_read_b64_tr_b16 v[156:157], v177 offset:0x6800
	ds_read_b64_tr_b16 v[158:159], v177 offset:0x7800
	s_waitcnt lgkmcnt(6)
	v_mfma_f32_32x32x16_bf16 v[48:63], v[144:147], v[128:131], v[48:63]
	ds_read_b64_tr_b16 v[192:193], v177 offset:0xa00
	ds_read_b64_tr_b16 v[194:195], v177 offset:0x1a00
	s_waitcnt lgkmcnt(6)
	v_mfma_f32_32x32x16_bf16 v[48:63], v[148:151], v[132:135], v[48:63]
	ds_read_b64_tr_b16 v[196:197], v177 offset:0x2a00
	ds_read_b64_tr_b16 v[198:199], v177 offset:0x3a00
	s_waitcnt lgkmcnt(6)
	v_mfma_f32_32x32x16_bf16 v[48:63], v[152:155], v[136:139], v[48:63]
	ds_read_b64_tr_b16 v[200:201], v177 offset:0x4a00
	ds_read_b64_tr_b16 v[202:203], v177 offset:0x5a00
	s_waitcnt lgkmcnt(6)
	v_mfma_f32_32x32x16_bf16 v[48:63], v[156:159], v[140:143], v[48:63]
	ds_read_b64_tr_b16 v[204:205], v177 offset:0x6a00
	ds_read_b64_tr_b16 v[206:207], v177 offset:0x7a00
	s_waitcnt lgkmcnt(6)
	v_mfma_f32_32x32x16_bf16 v[32:47], v[192:195], v[128:131], v[32:47]
	ds_read_b64_tr_b16 v[144:145], v177 offset:0xc00
	ds_read_b64_tr_b16 v[146:147], v177 offset:0x1c00
	s_waitcnt lgkmcnt(6)
	v_mfma_f32_32x32x16_bf16 v[32:47], v[196:199], v[132:135], v[32:47]
	ds_read_b64_tr_b16 v[148:149], v177 offset:0x2c00
	ds_read_b64_tr_b16 v[150:151], v177 offset:0x3c00
	s_waitcnt lgkmcnt(6)
	v_mfma_f32_32x32x16_bf16 v[32:47], v[200:203], v[136:139], v[32:47]
	ds_read_b64_tr_b16 v[152:153], v177 offset:0x4c00
	ds_read_b64_tr_b16 v[154:155], v177 offset:0x5c00
	s_waitcnt lgkmcnt(6)
	v_mfma_f32_32x32x16_bf16 v[32:47], v[204:207], v[140:143], v[32:47]
	ds_read_b64_tr_b16 v[156:157], v177 offset:0x6c00
	ds_read_b64_tr_b16 v[158:159], v177 offset:0x7c00
	s_waitcnt lgkmcnt(6)
	v_mfma_f32_32x32x16_bf16 v[16:31], v[144:147], v[128:131], v[16:31]
	ds_read_b64_tr_b16 v[192:193], v177 offset:0xe00
	ds_read_b64_tr_b16 v[194:195], v177 offset:0x1e00
	s_waitcnt lgkmcnt(6)
	v_mfma_f32_32x32x16_bf16 v[16:31], v[148:151], v[132:135], v[16:31]
	ds_read_b64_tr_b16 v[196:197], v177 offset:0x2e00
	ds_read_b64_tr_b16 v[198:199], v177 offset:0x3e00
	s_waitcnt lgkmcnt(6)
	v_mfma_f32_32x32x16_bf16 v[16:31], v[152:155], v[136:139], v[16:31]
	ds_read_b64_tr_b16 v[200:201], v177 offset:0x4e00
	ds_read_b64_tr_b16 v[202:203], v177 offset:0x5e00
	s_waitcnt lgkmcnt(6)
	v_mfma_f32_32x32x16_bf16 v[16:31], v[156:159], v[140:143], v[16:31]
	ds_read_b64_tr_b16 v[204:205], v177 offset:0x6e00
	ds_read_b64_tr_b16 v[206:207], v177 offset:0x7e00
	s_waitcnt lgkmcnt(6)
	v_mfma_f32_32x32x16_bf16 v[0:15], v[192:195], v[128:131], v[0:15]
	s_waitcnt lgkmcnt(4)
	v_mfma_f32_32x32x16_bf16 v[0:15], v[196:199], v[132:135], v[0:15]
	s_waitcnt lgkmcnt(2)
	v_mfma_f32_32x32x16_bf16 v[0:15], v[200:203], v[136:139], v[0:15]
	s_waitcnt lgkmcnt(0)
	v_mfma_f32_32x32x16_bf16 v[0:15], v[204:207], v[140:143], v[0:15]
	ds_read_b128 v[128:131], v188 offset:0
	ds_read_b128 v[132:135], v188 offset:0x2000
	ds_read_b128 v[192:195], v187 offset:0
	ds_read_b128 v[196:199], v187 offset:0x2000
	s_waitcnt lgkmcnt(2)
	s_nop 0
	v_mfma_f32_32x32x16_bf16 v[144:159], v[128:131], v[218:221], 0
	v_mfma_f32_32x32x16_bf16 v[128:143], v[132:135], v[218:221], 0
	ds_read_b128 v[204:207], v186 offset:0
	ds_read_b128 v[208:211], v186 offset:0x2000
	s_waitcnt lgkmcnt(2)
	v_mfma_f32_32x32x16_bf16 v[144:159], v[192:195], v[222:225], v[144:159]
	v_mfma_f32_32x32x16_bf16 v[128:143], v[196:199], v[222:225], v[128:143]
	ds_read_b128 v[192:195], v185 offset:0
	ds_read_b128 v[196:199], v185 offset:0x2000
	s_waitcnt lgkmcnt(2)
	v_mfma_f32_32x32x16_bf16 v[144:159], v[204:207], v[230:233], v[144:159]
	v_mfma_f32_32x32x16_bf16 v[128:143], v[208:211], v[230:233], v[128:143]
	ds_read_b128 v[204:207], v188 offset:0x80
	ds_read_b128 v[208:211], v188 offset:0x2080
	s_waitcnt lgkmcnt(2)
	v_mfma_f32_32x32x16_bf16 v[144:159], v[192:195], v[234:237], v[144:159]
	v_mfma_f32_32x32x16_bf16 v[128:143], v[196:199], v[234:237], v[128:143]
	ds_read_b128 v[192:195], v187 offset:0x80
	ds_read_b128 v[196:199], v187 offset:0x2080
	s_waitcnt lgkmcnt(2)
	v_mfma_f32_32x32x16_bf16 v[144:159], v[204:207], v[238:241], v[144:159]
	v_mfma_f32_32x32x16_bf16 v[128:143], v[208:211], v[238:241], v[128:143]
	ds_read_b128 v[204:207], v186 offset:0x80
	ds_read_b128 v[208:211], v186 offset:0x2080
	s_waitcnt lgkmcnt(2)
	v_mfma_f32_32x32x16_bf16 v[144:159], v[192:195], v[242:245], v[144:159]
	v_mfma_f32_32x32x16_bf16 v[128:143], v[196:199], v[242:245], v[128:143]
	ds_read_b128 v[180:183], v185 offset:0x80
	ds_read_b128 v[192:195], v185 offset:0x2080
	s_waitcnt lgkmcnt(2)
	v_mfma_f32_32x32x16_bf16 v[144:159], v[204:207], v[246:249], v[144:159]
	v_mfma_f32_32x32x16_bf16 v[128:143], v[208:211], v[246:249], v[128:143]
	s_waitcnt lgkmcnt(0)
	v_mfma_f32_32x32x16_bf16 v[144:159], v[180:183], v[166:169], v[144:159]
	v_mfma_f32_32x32x16_bf16 v[128:143], v[192:195], v[166:169], v[128:143]
	s_bitcmp0_b32 s100, 8
	s_cbranch_scc1 .Lstg_a20
	s_waitcnt vmcnt(0)
	s_waitcnt lgkmcnt(0)
	s_barrier
	s_sleep 7
